# v62 + LDS XOR-swizzle of SGU transposed tile (16B token chunk ^ (row>>4)&3) on ds_write_b16 writers and ds_read_b128 readers: removes 4/8-way bank conflict
# speedup vs baseline: 1.0081x; 1.0077x over previous
.LBB0_488:
	s_or_b64 exec, exec, s[20:21]
	s_lshl_b64 s[4:5], s[52:53], 2
	s_add_u32 s13, s18, s4
	s_addc_u32 s21, s19, s5
	v_readlane_b32 s4, v255, 23
	v_readlane_b32 s5, v255, 24
	s_lshl_b64 s[4:5], s[4:5], 2
	s_add_u32 s16, s16, s4
	s_addc_u32 s17, s17, s5
	s_add_u32 s18, s10, 0x27c20000
	s_mul_i32 s4, s12, 0x4400
	s_addc_u32 s19, s11, 0
	s_add_i32 s20, s4, 0
	s_lshl_b64 s[4:5], s[6:7], 2
	v_lshlrev_b32_e32 v2, 3, v144
	s_add_u32 s4, s13, s4
	s_addc_u32 s5, s21, s5
	v_lshlrev_b32_e32 v6, 2, v2
	s_waitcnt lgkmcnt(0)
	s_barrier
	global_load_dwordx4 v[2:5], v6, s[4:5] offset:16
	s_nop 0
	global_load_dwordx4 v[6:9], v6, s[4:5]
	s_add_i32 s7, 0, 0x22000
	v_lshl_add_u32 v161, v0, 5, s7
	ds_read_b128 v[162:165], v161
	ds_read_b128 v[166:169], v161 offset:16
	v_and_b32_e32 v103, 63, v87
	v_and_b32_e32 v105, 31, v87
	v_or_b32_e32 v160, 8, v0
	s_waitcnt lgkmcnt(1)
	v_add_f32_e32 v161, v162, v163
	v_add_f32_e32 v162, v164, v165
	v_add_f32_e32 v161, v161, v162
	s_waitcnt lgkmcnt(0)
	v_add_f32_e32 v162, v166, v167
	v_add_f32_e32 v161, v161, v162
	v_add_f32_e32 v162, v168, v169
	v_add_f32_e32 v161, v162, v161
	v_fmamk_f32 v161, v161, 0x3b000000, v235
	v_rsq_f32_e32 v161, v161
	v_or_b32_e32 v159, 16, v0
	v_or_b32_e32 v150, 24, v0
	v_or_b32_e32 v149, 32, v0
	v_mul_f32_e32 v151, v161, v151
	v_or_b32_e32 v148, 40, v0
	v_or_b32_e32 v147, 48, v0
	v_or_b32_e32 v146, 56, v0
	v_or_b32_e32 v145, 64, v0
	v_or_b32_e32 v143, 0x48, v0
	v_or_b32_e32 v134, 0x50, v0
	v_or_b32_e32 v133, 0x58, v0
	v_or_b32_e32 v132, 0x60, v0
	v_or_b32_e32 v128, 0x68, v0
	v_or_b32_e32 v87, 0x70, v0
	v_or_b32_e32 v49, 0x78, v0
	v_mul_f32_e32 v152, v161, v152
	v_mul_f32_e32 v154, v161, v154
	v_mul_f32_e32 v153, v161, v153
	v_mul_f32_e32 v156, v161, v156
	v_mul_f32_e32 v155, v161, v155
	v_mul_f32_e32 v158, v161, v158
	v_mul_f32_e32 v157, v161, v157
	v_lshlrev_b32_e32 v161, 1, v0
	v_mul_u32_u24_e32 v0, 0x880, v144
	v_lshrrev_b32_e32 v144, 1, v144
	v_lshl_add_u32 v161, v144, 4, v161
	v_add3_u32 v144, s20, v161, v0
	s_ashr_i32 s13, s12, 31
	s_lshl_b64 s[4:5], s[12:13], 15
	v_lshrrev_b32_e32 v106, 5, v103
	s_add_u32 s4, s10, s4
	s_addc_u32 s5, s11, s5
	s_lshl_b32 s23, s12, 4
	s_waitcnt vmcnt(1)
	v_mul_f32_e32 v156, v2, v156
	s_waitcnt vmcnt(0)
	v_mul_f32_e32 v151, v7, v151
	v_mul_f32_e32 v154, v8, v154
	v_cvt_pk_bf16_f32 v151, v151, s0
	v_mul_f32_e32 v153, v9, v153
	ds_write_b16 v144, v151 offset:272
	v_cvt_pk_bf16_f32 v151, v154, s0
	ds_write_b16 v144, v151 offset:544
	v_cvt_pk_bf16_f32 v151, v153, s0
	v_mul_f32_e32 v155, v3, v155
	ds_write_b16 v144, v151 offset:816
	v_cvt_pk_bf16_f32 v151, v156, s0
	v_mul_f32_e32 v158, v4, v158
	ds_write_b16 v144, v151 offset:1088
	v_cvt_pk_bf16_f32 v151, v155, s0
	v_mul_f32_e32 v152, v6, v152
	v_mul_f32_e32 v157, v5, v157
	ds_write_b16 v144, v151 offset:1360
	v_cvt_pk_bf16_f32 v151, v158, s0
	v_cvt_pk_bf16_f32 v152, v152, s0
	ds_write_b16 v144, v151 offset:1632
	v_cvt_pk_bf16_f32 v151, v157, s0
	ds_write_b16 v144, v152
	ds_write_b16 v144, v151 offset:1904
	v_lshl_add_u32 v144, v160, 5, s7
	ds_read_b128 v[152:155], v144
	ds_read_b128 v[162:165], v144 offset:16
	s_waitcnt lgkmcnt(1)
	v_add_f32_e32 v144, v152, v153
	v_add_f32_e32 v151, v154, v155
	v_add_f32_e32 v144, v144, v151
	s_waitcnt lgkmcnt(0)
	v_add_f32_e32 v151, v162, v163
	v_add_f32_e32 v144, v144, v151
	v_add_f32_e32 v151, v164, v165
	v_add_f32_e32 v144, v151, v144
	v_fmamk_f32 v144, v144, 0x3b000000, v235
	v_rsq_f32_e32 v144, v144
	s_nop 0
	v_mul_f32_e32 v135, v144, v135
	v_mul_f32_e32 v136, v144, v136
	v_mul_f32_e32 v135, v7, v135
	v_mul_f32_e32 v138, v144, v138
	v_mul_f32_e32 v137, v144, v137
	v_mul_f32_e32 v140, v144, v140
	v_mul_f32_e32 v139, v144, v139
	v_mul_f32_e32 v142, v144, v142
	v_mul_f32_e32 v141, v144, v141
	v_bfe_u32 v144, v0, 8, 2
	v_lshlrev_b32_e32 v144, 3, v144
	v_xor_b32_e32 v144, v144, v160
	v_lshlrev_b32_e32 v144, 1, v144
	v_mul_f32_e32 v138, v8, v138
	v_add3_u32 v144, s20, v144, v0
	v_cvt_pk_bf16_f32 v135, v135, s0
	v_mul_f32_e32 v137, v9, v137
	ds_write_b16 v144, v135 offset:272
	v_cvt_pk_bf16_f32 v135, v138, s0
	v_mul_f32_e32 v140, v2, v140
	ds_write_b16 v144, v135 offset:544
	v_cvt_pk_bf16_f32 v135, v137, s0
	v_mul_f32_e32 v139, v3, v139
	ds_write_b16 v144, v135 offset:816
	v_cvt_pk_bf16_f32 v135, v140, s0
	v_mul_f32_e32 v142, v4, v142
	ds_write_b16 v144, v135 offset:1088
	v_cvt_pk_bf16_f32 v135, v139, s0
	v_mul_f32_e32 v136, v6, v136
	v_mul_f32_e32 v141, v5, v141
	ds_write_b16 v144, v135 offset:1360
	v_cvt_pk_bf16_f32 v135, v142, s0
	v_cvt_pk_bf16_f32 v136, v136, s0
	ds_write_b16 v144, v135 offset:1632
	v_cvt_pk_bf16_f32 v135, v141, s0
	ds_write_b16 v144, v136
	ds_write_b16 v144, v135 offset:1904
	v_lshl_add_u32 v135, v159, 5, s7
	ds_read_b128 v[136:139], v135
	ds_read_b128 v[152:155], v135 offset:16
	s_waitcnt lgkmcnt(1)
	v_add_f32_e32 v135, v136, v137
	v_add_f32_e32 v136, v138, v139
	v_add_f32_e32 v135, v135, v136
	s_waitcnt lgkmcnt(0)
	v_add_f32_e32 v136, v152, v153
	v_add_f32_e32 v135, v135, v136
	v_add_f32_e32 v136, v154, v155
	v_add_f32_e32 v135, v136, v135
	v_fmamk_f32 v135, v135, 0x3b000000, v235
	v_rsq_f32_e32 v135, v135
	s_nop 0
	v_mul_f32_e32 v123, v135, v123
	v_mul_f32_e32 v124, v135, v124
	v_mul_f32_e32 v123, v7, v123
	v_mul_f32_e32 v126, v135, v126
	v_mul_f32_e32 v125, v135, v125
	v_mul_f32_e32 v129, v135, v129
	v_mul_f32_e32 v127, v135, v127
	v_mul_f32_e32 v131, v135, v131
	v_mul_f32_e32 v130, v135, v130
	v_bfe_u32 v135, v0, 8, 2
	v_lshlrev_b32_e32 v135, 3, v135
	v_xor_b32_e32 v135, v135, v159
	v_lshlrev_b32_e32 v135, 1, v135
	v_mul_f32_e32 v126, v8, v126
	v_add3_u32 v135, s20, v135, v0
	v_cvt_pk_bf16_f32 v123, v123, s0
	v_mul_f32_e32 v125, v9, v125
	ds_write_b16 v135, v123 offset:272
	v_cvt_pk_bf16_f32 v123, v126, s0
	v_mul_f32_e32 v129, v2, v129
	ds_write_b16 v135, v123 offset:544
	v_cvt_pk_bf16_f32 v123, v125, s0
	v_mul_f32_e32 v127, v3, v127
	ds_write_b16 v135, v123 offset:816
	v_cvt_pk_bf16_f32 v123, v129, s0
	v_mul_f32_e32 v131, v4, v131
	ds_write_b16 v135, v123 offset:1088
	v_cvt_pk_bf16_f32 v123, v127, s0
	v_mul_f32_e32 v124, v6, v124
	v_mul_f32_e32 v130, v5, v130
	ds_write_b16 v135, v123 offset:1360
	v_cvt_pk_bf16_f32 v123, v131, s0
	v_cvt_pk_bf16_f32 v124, v124, s0
	ds_write_b16 v135, v123 offset:1632
	v_cvt_pk_bf16_f32 v123, v130, s0
	ds_write_b16 v135, v124
	ds_write_b16 v135, v123 offset:1904
	v_lshl_add_u32 v123, v150, 5, s7
	ds_read_b128 v[124:127], v123
	ds_read_b128 v[136:139], v123 offset:16
	s_waitcnt lgkmcnt(1)
	v_add_f32_e32 v123, v124, v125
	v_add_f32_e32 v124, v126, v127
	v_add_f32_e32 v123, v123, v124
	s_waitcnt lgkmcnt(0)
	v_add_f32_e32 v124, v136, v137
	v_add_f32_e32 v123, v123, v124
	v_add_f32_e32 v124, v138, v139
	v_add_f32_e32 v123, v124, v123
	v_fmamk_f32 v123, v123, 0x3b000000, v235
	v_rsq_f32_e32 v123, v123
	s_nop 0
	v_mul_f32_e32 v115, v123, v115
	v_mul_f32_e32 v116, v123, v116
	v_mul_f32_e32 v115, v7, v115
	v_mul_f32_e32 v118, v123, v118
	v_mul_f32_e32 v117, v123, v117
	v_mul_f32_e32 v120, v123, v120
	v_mul_f32_e32 v119, v123, v119
	v_mul_f32_e32 v122, v123, v122
	v_mul_f32_e32 v121, v123, v121
	v_bfe_u32 v123, v0, 8, 2
	v_lshlrev_b32_e32 v123, 3, v123
	v_xor_b32_e32 v123, v123, v150
	v_lshlrev_b32_e32 v123, 1, v123
	v_mul_f32_e32 v118, v8, v118
	v_add3_u32 v123, s20, v123, v0
	v_cvt_pk_bf16_f32 v115, v115, s0
	v_mul_f32_e32 v117, v9, v117
	ds_write_b16 v123, v115 offset:272
	v_cvt_pk_bf16_f32 v115, v118, s0
	v_mul_f32_e32 v120, v2, v120
	ds_write_b16 v123, v115 offset:544
	v_cvt_pk_bf16_f32 v115, v117, s0
	v_mul_f32_e32 v119, v3, v119
	ds_write_b16 v123, v115 offset:816
	v_cvt_pk_bf16_f32 v115, v120, s0
	v_mul_f32_e32 v122, v4, v122
	ds_write_b16 v123, v115 offset:1088
	v_cvt_pk_bf16_f32 v115, v119, s0
	v_mul_f32_e32 v116, v6, v116
	v_mul_f32_e32 v121, v5, v121
	ds_write_b16 v123, v115 offset:1360
	v_cvt_pk_bf16_f32 v115, v122, s0
	v_cvt_pk_bf16_f32 v116, v116, s0
	ds_write_b16 v123, v115 offset:1632
	v_cvt_pk_bf16_f32 v115, v121, s0
	ds_write_b16 v123, v116
	ds_write_b16 v123, v115 offset:1904
	v_lshl_add_u32 v115, v149, 5, s7
	ds_read_b128 v[116:119], v115
	ds_read_b128 v[120:123], v115 offset:16
	s_waitcnt lgkmcnt(1)
	v_add_f32_e32 v115, v116, v117
	v_add_f32_e32 v116, v118, v119
	v_add_f32_e32 v115, v115, v116
	s_waitcnt lgkmcnt(0)
	v_add_f32_e32 v116, v120, v121
	v_add_f32_e32 v115, v115, v116
	v_add_f32_e32 v116, v122, v123
	v_add_f32_e32 v115, v116, v115
	v_fmamk_f32 v115, v115, 0x3b000000, v235
	v_rsq_f32_e32 v115, v115
	s_nop 0
	v_mul_f32_e32 v107, v115, v107
	v_mul_f32_e32 v108, v115, v108
	v_mul_f32_e32 v107, v7, v107
	v_mul_f32_e32 v110, v115, v110
	v_mul_f32_e32 v109, v115, v109
	v_mul_f32_e32 v112, v115, v112
	v_mul_f32_e32 v111, v115, v111
	v_mul_f32_e32 v114, v115, v114
	v_mul_f32_e32 v113, v115, v113
	v_bfe_u32 v115, v0, 8, 2
	v_lshlrev_b32_e32 v115, 3, v115
	v_xor_b32_e32 v115, v115, v149
	v_lshlrev_b32_e32 v115, 1, v115
	v_mul_f32_e32 v110, v8, v110
	v_add3_u32 v115, s20, v115, v0
	v_cvt_pk_bf16_f32 v107, v107, s0
	v_mul_f32_e32 v109, v9, v109
	ds_write_b16 v115, v107 offset:272
	v_cvt_pk_bf16_f32 v107, v110, s0
	v_mul_f32_e32 v112, v2, v112
	ds_write_b16 v115, v107 offset:544
	v_cvt_pk_bf16_f32 v107, v109, s0
	v_mul_f32_e32 v111, v3, v111
	ds_write_b16 v115, v107 offset:816
	v_cvt_pk_bf16_f32 v107, v112, s0
	v_mul_f32_e32 v114, v4, v114
	ds_write_b16 v115, v107 offset:1088
	v_cvt_pk_bf16_f32 v107, v111, s0
	v_mul_f32_e32 v108, v6, v108
	v_mul_f32_e32 v113, v5, v113
	ds_write_b16 v115, v107 offset:1360
	v_cvt_pk_bf16_f32 v107, v114, s0
	v_cvt_pk_bf16_f32 v108, v108, s0
	ds_write_b16 v115, v107 offset:1632
	v_cvt_pk_bf16_f32 v107, v113, s0
	ds_write_b16 v115, v108
	ds_write_b16 v115, v107 offset:1904
	v_lshl_add_u32 v107, v148, 5, s7
	ds_read_b128 v[108:111], v107
	ds_read_b128 v[112:115], v107 offset:16
	s_waitcnt lgkmcnt(1)
	v_add_f32_e32 v107, v108, v109
	v_add_f32_e32 v108, v110, v111
	v_add_f32_e32 v107, v107, v108
	s_waitcnt lgkmcnt(0)
	v_add_f32_e32 v108, v112, v113
	v_add_f32_e32 v107, v107, v108
	v_add_f32_e32 v108, v114, v115
	v_add_f32_e32 v107, v108, v107
	v_fmamk_f32 v107, v107, 0x3b000000, v235
	v_rsq_f32_e32 v107, v107
	s_nop 0
	v_mul_f32_e32 v92, v107, v92
	v_mul_f32_e32 v93, v107, v93
	v_mul_f32_e32 v92, v7, v92
	v_mul_f32_e32 v95, v107, v95
	v_mul_f32_e32 v94, v107, v94
	v_mul_f32_e32 v97, v107, v97
	v_mul_f32_e32 v96, v107, v96
	v_mul_f32_e32 v99, v107, v99
	v_mul_f32_e32 v98, v107, v98
	v_bfe_u32 v107, v0, 8, 2
	v_lshlrev_b32_e32 v107, 3, v107
	v_xor_b32_e32 v107, v107, v148
	v_lshlrev_b32_e32 v107, 1, v107
	v_mul_f32_e32 v95, v8, v95
	v_add3_u32 v107, s20, v107, v0
	v_cvt_pk_bf16_f32 v92, v92, s0
	v_mul_f32_e32 v94, v9, v94
	ds_write_b16 v107, v92 offset:272
	v_cvt_pk_bf16_f32 v92, v95, s0
	v_mul_f32_e32 v97, v2, v97
	ds_write_b16 v107, v92 offset:544
	v_cvt_pk_bf16_f32 v92, v94, s0
	v_mul_f32_e32 v96, v3, v96
	ds_write_b16 v107, v92 offset:816
	v_cvt_pk_bf16_f32 v92, v97, s0
	v_mul_f32_e32 v99, v4, v99
	ds_write_b16 v107, v92 offset:1088
	v_cvt_pk_bf16_f32 v92, v96, s0
	v_mul_f32_e32 v93, v6, v93
	v_mul_f32_e32 v98, v5, v98
	ds_write_b16 v107, v92 offset:1360
	v_cvt_pk_bf16_f32 v92, v99, s0
	v_cvt_pk_bf16_f32 v93, v93, s0
	ds_write_b16 v107, v92 offset:1632
	v_cvt_pk_bf16_f32 v92, v98, s0
	ds_write_b16 v107, v93
	ds_write_b16 v107, v92 offset:1904
	v_lshl_add_u32 v96, v147, 5, s7
	ds_read_b128 v[92:95], v96
	ds_read_b128 v[96:99], v96 offset:16
	s_waitcnt lgkmcnt(1)
	v_add_f32_e32 v92, v92, v93
	v_add_f32_e32 v93, v94, v95
	v_add_f32_e32 v92, v92, v93
	s_waitcnt lgkmcnt(0)
	v_add_f32_e32 v93, v96, v97
	v_add_f32_e32 v92, v92, v93
	v_add_f32_e32 v93, v98, v99
	v_add_f32_e32 v92, v93, v92
	v_fmamk_f32 v92, v92, 0x3b000000, v235
	v_rsq_f32_e32 v92, v92
	s_nop 0
	v_mul_f32_e32 v83, v92, v83
	v_mul_f32_e32 v84, v92, v84
	v_mul_f32_e32 v83, v7, v83
	v_mul_f32_e32 v86, v92, v86
	v_mul_f32_e32 v85, v92, v85
	v_mul_f32_e32 v89, v92, v89
	v_mul_f32_e32 v88, v92, v88
	v_mul_f32_e32 v91, v92, v91
	v_mul_f32_e32 v90, v92, v90
	v_bfe_u32 v92, v0, 8, 2
	v_lshlrev_b32_e32 v92, 3, v92
	v_xor_b32_e32 v92, v92, v147
	v_lshlrev_b32_e32 v92, 1, v92
	v_mul_f32_e32 v86, v8, v86
	v_add3_u32 v92, s20, v92, v0
	v_cvt_pk_bf16_f32 v83, v83, s0
	v_mul_f32_e32 v85, v9, v85
	ds_write_b16 v92, v83 offset:272
	v_cvt_pk_bf16_f32 v83, v86, s0
	v_mul_f32_e32 v89, v2, v89
	ds_write_b16 v92, v83 offset:544
	v_cvt_pk_bf16_f32 v83, v85, s0
	v_mul_f32_e32 v88, v3, v88
	ds_write_b16 v92, v83 offset:816
	v_cvt_pk_bf16_f32 v83, v89, s0
	v_mul_f32_e32 v91, v4, v91
	ds_write_b16 v92, v83 offset:1088
	v_cvt_pk_bf16_f32 v83, v88, s0
	v_mul_f32_e32 v84, v6, v84
	v_mul_f32_e32 v90, v5, v90
	ds_write_b16 v92, v83 offset:1360
	v_cvt_pk_bf16_f32 v83, v91, s0
	v_cvt_pk_bf16_f32 v84, v84, s0
	ds_write_b16 v92, v83 offset:1632
	v_cvt_pk_bf16_f32 v83, v90, s0
	ds_write_b16 v92, v84
	ds_write_b16 v92, v83 offset:1904
	v_lshl_add_u32 v83, v146, 5, s7
	ds_read_b128 v[88:91], v83
	ds_read_b128 v[92:95], v83 offset:16
	s_waitcnt lgkmcnt(1)
	v_add_f32_e32 v83, v88, v89
	v_add_f32_e32 v84, v90, v91
	v_add_f32_e32 v83, v83, v84
	s_waitcnt lgkmcnt(0)
	v_add_f32_e32 v84, v92, v93
	v_add_f32_e32 v83, v83, v84
	v_add_f32_e32 v84, v94, v95
	v_add_f32_e32 v83, v84, v83
	v_fmamk_f32 v83, v83, 0x3b000000, v235
	v_rsq_f32_e32 v83, v83
	s_nop 0
	v_mul_f32_e32 v75, v83, v75
	v_mul_f32_e32 v76, v83, v76
	v_mul_f32_e32 v75, v7, v75
	v_mul_f32_e32 v78, v83, v78
	v_mul_f32_e32 v77, v83, v77
	v_mul_f32_e32 v80, v83, v80
	v_mul_f32_e32 v79, v83, v79
	v_mul_f32_e32 v82, v83, v82
	v_mul_f32_e32 v81, v83, v81
	v_bfe_u32 v83, v0, 8, 2
	v_lshlrev_b32_e32 v83, 3, v83
	v_xor_b32_e32 v83, v83, v146
	v_lshlrev_b32_e32 v83, 1, v83
	v_mul_f32_e32 v78, v8, v78
	v_add3_u32 v83, s20, v83, v0
	v_cvt_pk_bf16_f32 v75, v75, s0
	v_mul_f32_e32 v77, v9, v77
	ds_write_b16 v83, v75 offset:272
	v_cvt_pk_bf16_f32 v75, v78, s0
	v_mul_f32_e32 v80, v2, v80
	ds_write_b16 v83, v75 offset:544
	v_cvt_pk_bf16_f32 v75, v77, s0
	v_mul_f32_e32 v79, v3, v79
	ds_write_b16 v83, v75 offset:816
	v_cvt_pk_bf16_f32 v75, v80, s0
	v_mul_f32_e32 v82, v4, v82
	ds_write_b16 v83, v75 offset:1088
	v_cvt_pk_bf16_f32 v75, v79, s0
	v_mul_f32_e32 v76, v6, v76
	v_mul_f32_e32 v81, v5, v81
	ds_write_b16 v83, v75 offset:1360
	v_cvt_pk_bf16_f32 v75, v82, s0
	v_cvt_pk_bf16_f32 v76, v76, s0
	ds_write_b16 v83, v75 offset:1632
	v_cvt_pk_bf16_f32 v75, v81, s0
	ds_write_b16 v83, v76
	ds_write_b16 v83, v75 offset:1904
	v_lshl_add_u32 v75, v145, 5, s7
	ds_read_b128 v[76:79], v75
	ds_read_b128 v[80:83], v75 offset:16
	s_waitcnt lgkmcnt(1)
	v_add_f32_e32 v75, v76, v77
	v_add_f32_e32 v76, v78, v79
	v_add_f32_e32 v75, v75, v76
	s_waitcnt lgkmcnt(0)
	v_add_f32_e32 v76, v80, v81
	v_add_f32_e32 v75, v75, v76
	v_add_f32_e32 v76, v82, v83
	v_add_f32_e32 v75, v76, v75
	v_fmamk_f32 v75, v75, 0x3b000000, v235
	v_rsq_f32_e32 v75, v75
	s_nop 0
	v_mul_f32_e32 v67, v75, v67
	v_mul_f32_e32 v68, v75, v68
	v_mul_f32_e32 v67, v7, v67
	v_mul_f32_e32 v70, v75, v70
	v_mul_f32_e32 v69, v75, v69
	v_mul_f32_e32 v72, v75, v72
	v_mul_f32_e32 v71, v75, v71
	v_mul_f32_e32 v74, v75, v74
	v_mul_f32_e32 v73, v75, v73
	v_bfe_u32 v75, v0, 8, 2
	v_lshlrev_b32_e32 v75, 3, v75
	v_xor_b32_e32 v75, v75, v145
	v_lshlrev_b32_e32 v75, 1, v75
	v_mul_f32_e32 v70, v8, v70
	v_add3_u32 v75, s20, v75, v0
	v_cvt_pk_bf16_f32 v67, v67, s0
	v_mul_f32_e32 v69, v9, v69
	ds_write_b16 v75, v67 offset:272
	v_cvt_pk_bf16_f32 v67, v70, s0
	v_mul_f32_e32 v72, v2, v72
	ds_write_b16 v75, v67 offset:544
	v_cvt_pk_bf16_f32 v67, v69, s0
	v_mul_f32_e32 v71, v3, v71
	ds_write_b16 v75, v67 offset:816
	v_cvt_pk_bf16_f32 v67, v72, s0
	v_mul_f32_e32 v74, v4, v74
	ds_write_b16 v75, v67 offset:1088
	v_cvt_pk_bf16_f32 v67, v71, s0
	v_mul_f32_e32 v68, v6, v68
	v_mul_f32_e32 v73, v5, v73
	ds_write_b16 v75, v67 offset:1360
	v_cvt_pk_bf16_f32 v67, v74, s0
	v_cvt_pk_bf16_f32 v68, v68, s0
	ds_write_b16 v75, v67 offset:1632
	v_cvt_pk_bf16_f32 v67, v73, s0
	ds_write_b16 v75, v68
	ds_write_b16 v75, v67 offset:1904
	v_lshl_add_u32 v67, v143, 5, s7
	ds_read_b128 v[68:71], v67
	ds_read_b128 v[72:75], v67 offset:16
	s_waitcnt lgkmcnt(1)
	v_add_f32_e32 v67, v68, v69
	v_add_f32_e32 v68, v70, v71
	v_add_f32_e32 v67, v67, v68
	s_waitcnt lgkmcnt(0)
	v_add_f32_e32 v68, v72, v73
	v_add_f32_e32 v67, v67, v68
	v_add_f32_e32 v68, v74, v75
	v_add_f32_e32 v67, v68, v67
	v_fmamk_f32 v67, v67, 0x3b000000, v235
	v_rsq_f32_e32 v67, v67
	s_nop 0
	v_mul_f32_e32 v59, v67, v59
	v_mul_f32_e32 v60, v67, v60
	v_mul_f32_e32 v59, v7, v59
	v_mul_f32_e32 v62, v67, v62
	v_mul_f32_e32 v61, v67, v61
	v_mul_f32_e32 v64, v67, v64
	v_mul_f32_e32 v63, v67, v63
	v_mul_f32_e32 v66, v67, v66
	v_mul_f32_e32 v65, v67, v65
	v_bfe_u32 v67, v0, 8, 2
	v_lshlrev_b32_e32 v67, 3, v67
	v_xor_b32_e32 v67, v67, v143
	v_lshlrev_b32_e32 v67, 1, v67
	v_mul_f32_e32 v62, v8, v62
	v_add3_u32 v67, s20, v67, v0
	v_cvt_pk_bf16_f32 v59, v59, s0
	v_mul_f32_e32 v61, v9, v61
	ds_write_b16 v67, v59 offset:272
	v_cvt_pk_bf16_f32 v59, v62, s0
	v_mul_f32_e32 v64, v2, v64
	ds_write_b16 v67, v59 offset:544
	v_cvt_pk_bf16_f32 v59, v61, s0
	v_mul_f32_e32 v63, v3, v63
	ds_write_b16 v67, v59 offset:816
	v_cvt_pk_bf16_f32 v59, v64, s0
	v_mul_f32_e32 v66, v4, v66
	ds_write_b16 v67, v59 offset:1088
	v_cvt_pk_bf16_f32 v59, v63, s0
	v_mul_f32_e32 v60, v6, v60
	v_mul_f32_e32 v65, v5, v65
	ds_write_b16 v67, v59 offset:1360
	v_cvt_pk_bf16_f32 v59, v66, s0
	v_cvt_pk_bf16_f32 v60, v60, s0
	ds_write_b16 v67, v59 offset:1632
	v_cvt_pk_bf16_f32 v59, v65, s0
	ds_write_b16 v67, v60
	ds_write_b16 v67, v59 offset:1904
	v_lshl_add_u32 v59, v134, 5, s7
	ds_read_b128 v[60:63], v59
	ds_read_b128 v[64:67], v59 offset:16
	s_waitcnt lgkmcnt(1)
	v_add_f32_e32 v59, v60, v61
	v_add_f32_e32 v60, v62, v63
	v_add_f32_e32 v59, v59, v60
	s_waitcnt lgkmcnt(0)
	v_add_f32_e32 v60, v64, v65
	v_add_f32_e32 v59, v59, v60
	v_add_f32_e32 v60, v66, v67
	v_add_f32_e32 v59, v60, v59
	v_fmamk_f32 v59, v59, 0x3b000000, v235
	v_rsq_f32_e32 v59, v59
	s_nop 0
	v_mul_f32_e32 v51, v59, v51
	v_mul_f32_e32 v52, v59, v52
	v_mul_f32_e32 v51, v7, v51
	v_mul_f32_e32 v54, v59, v54
	v_mul_f32_e32 v53, v59, v53
	v_mul_f32_e32 v56, v59, v56
	v_mul_f32_e32 v55, v59, v55
	v_mul_f32_e32 v58, v59, v58
	v_mul_f32_e32 v57, v59, v57
	v_bfe_u32 v59, v0, 8, 2
	v_lshlrev_b32_e32 v59, 3, v59
	v_xor_b32_e32 v59, v59, v134
	v_lshlrev_b32_e32 v59, 1, v59
	v_mul_f32_e32 v54, v8, v54
	v_add3_u32 v59, s20, v59, v0
	v_cvt_pk_bf16_f32 v51, v51, s0
	v_mul_f32_e32 v53, v9, v53
	ds_write_b16 v59, v51 offset:272
	v_cvt_pk_bf16_f32 v51, v54, s0
	v_mul_f32_e32 v56, v2, v56
	ds_write_b16 v59, v51 offset:544
	v_cvt_pk_bf16_f32 v51, v53, s0
	v_mul_f32_e32 v55, v3, v55
	ds_write_b16 v59, v51 offset:816
	v_cvt_pk_bf16_f32 v51, v56, s0
	v_mul_f32_e32 v58, v4, v58
	ds_write_b16 v59, v51 offset:1088
	v_cvt_pk_bf16_f32 v51, v55, s0
	v_mul_f32_e32 v52, v6, v52
	v_mul_f32_e32 v57, v5, v57
	ds_write_b16 v59, v51 offset:1360
	v_cvt_pk_bf16_f32 v51, v58, s0
	v_cvt_pk_bf16_f32 v52, v52, s0
	ds_write_b16 v59, v51 offset:1632
	v_cvt_pk_bf16_f32 v51, v57, s0
	ds_write_b16 v59, v52
	ds_write_b16 v59, v51 offset:1904
	v_lshl_add_u32 v51, v133, 5, s7
	ds_read_b128 v[52:55], v51
	ds_read_b128 v[56:59], v51 offset:16
	s_waitcnt lgkmcnt(1)
	v_add_f32_e32 v51, v52, v53
	v_add_f32_e32 v52, v54, v55
	v_add_f32_e32 v51, v51, v52
	s_waitcnt lgkmcnt(0)
	v_add_f32_e32 v52, v56, v57
	v_add_f32_e32 v51, v51, v52
	v_add_f32_e32 v52, v58, v59
	v_add_f32_e32 v51, v52, v51
	v_fmamk_f32 v51, v51, 0x3b000000, v235
	v_rsq_f32_e32 v51, v51
	s_nop 0
	v_mul_f32_e32 v42, v51, v42
	v_mul_f32_e32 v43, v51, v43
	v_mul_f32_e32 v42, v7, v42
	v_mul_f32_e32 v45, v51, v45
	v_mul_f32_e32 v44, v51, v44
	v_mul_f32_e32 v47, v51, v47
	v_mul_f32_e32 v46, v51, v46
	v_mul_f32_e32 v50, v51, v50
	v_mul_f32_e32 v48, v51, v48
	v_bfe_u32 v51, v0, 8, 2
	v_lshlrev_b32_e32 v51, 3, v51
	v_xor_b32_e32 v51, v51, v133
	v_lshlrev_b32_e32 v51, 1, v51
	v_mul_f32_e32 v45, v8, v45
	v_add3_u32 v51, s20, v51, v0
	v_cvt_pk_bf16_f32 v42, v42, s0
	v_mul_f32_e32 v44, v9, v44
	ds_write_b16 v51, v42 offset:272
	v_cvt_pk_bf16_f32 v42, v45, s0
	v_mul_f32_e32 v47, v2, v47
	ds_write_b16 v51, v42 offset:544
	v_cvt_pk_bf16_f32 v42, v44, s0
	v_mul_f32_e32 v46, v3, v46
	ds_write_b16 v51, v42 offset:816
	v_cvt_pk_bf16_f32 v42, v47, s0
	v_mul_f32_e32 v50, v4, v50
	ds_write_b16 v51, v42 offset:1088
	v_cvt_pk_bf16_f32 v42, v46, s0
	v_mul_f32_e32 v43, v6, v43
	v_mul_f32_e32 v48, v5, v48
	ds_write_b16 v51, v42 offset:1360
	v_cvt_pk_bf16_f32 v42, v50, s0
	v_cvt_pk_bf16_f32 v43, v43, s0
	ds_write_b16 v51, v42 offset:1632
	v_cvt_pk_bf16_f32 v42, v48, s0
	ds_write_b16 v51, v43
	ds_write_b16 v51, v42 offset:1904
	v_lshl_add_u32 v46, v132, 5, s7
	ds_read_b128 v[42:45], v46
	ds_read_b128 v[50:53], v46 offset:16
	s_waitcnt lgkmcnt(1)
	v_add_f32_e32 v42, v42, v43
	v_add_f32_e32 v43, v44, v45
	v_add_f32_e32 v42, v42, v43
	s_waitcnt lgkmcnt(0)
	v_add_f32_e32 v43, v50, v51
	v_add_f32_e32 v42, v42, v43
	v_add_f32_e32 v43, v52, v53
	v_add_f32_e32 v42, v43, v42
	v_fmamk_f32 v42, v42, 0x3b000000, v235
	v_rsq_f32_e32 v42, v42
	s_nop 0
	v_mul_f32_e32 v34, v42, v34
	v_mul_f32_e32 v35, v42, v35
	v_mul_f32_e32 v34, v7, v34
	v_mul_f32_e32 v37, v42, v37
	v_mul_f32_e32 v36, v42, v36
	v_mul_f32_e32 v39, v42, v39
	v_mul_f32_e32 v38, v42, v38
	v_mul_f32_e32 v41, v42, v41
	v_mul_f32_e32 v40, v42, v40
	v_bfe_u32 v42, v0, 8, 2
	v_lshlrev_b32_e32 v42, 3, v42
	v_xor_b32_e32 v42, v42, v132
	v_lshlrev_b32_e32 v42, 1, v42
	v_mul_f32_e32 v37, v8, v37
	v_add3_u32 v42, s20, v42, v0
	v_cvt_pk_bf16_f32 v34, v34, s0
	v_mul_f32_e32 v36, v9, v36
	ds_write_b16 v42, v34 offset:272
	v_cvt_pk_bf16_f32 v34, v37, s0
	v_mul_f32_e32 v39, v2, v39
	ds_write_b16 v42, v34 offset:544
	v_cvt_pk_bf16_f32 v34, v36, s0
	v_mul_f32_e32 v38, v3, v38
	ds_write_b16 v42, v34 offset:816
	v_cvt_pk_bf16_f32 v34, v39, s0
	v_mul_f32_e32 v41, v4, v41
	ds_write_b16 v42, v34 offset:1088
	v_cvt_pk_bf16_f32 v34, v38, s0
	v_mul_f32_e32 v35, v6, v35
	v_mul_f32_e32 v40, v5, v40
	ds_write_b16 v42, v34 offset:1360
	v_cvt_pk_bf16_f32 v34, v41, s0
	v_cvt_pk_bf16_f32 v35, v35, s0
	ds_write_b16 v42, v34 offset:1632
	v_cvt_pk_bf16_f32 v34, v40, s0
	ds_write_b16 v42, v35
	ds_write_b16 v42, v34 offset:1904
	v_lshl_add_u32 v38, v128, 5, s7
	ds_read_b128 v[34:37], v38
	ds_read_b128 v[38:41], v38 offset:16
	s_waitcnt lgkmcnt(1)
	v_add_f32_e32 v34, v34, v35
	v_add_f32_e32 v35, v36, v37
	v_add_f32_e32 v34, v34, v35
	s_waitcnt lgkmcnt(0)
	v_add_f32_e32 v35, v38, v39
	v_add_f32_e32 v34, v34, v35
	v_add_f32_e32 v35, v40, v41
	v_add_f32_e32 v34, v35, v34
	v_fmamk_f32 v34, v34, 0x3b000000, v235
	v_rsq_f32_e32 v34, v34
	s_nop 0
	v_mul_f32_e32 v26, v34, v26
	v_mul_f32_e32 v27, v34, v27
	v_mul_f32_e32 v26, v7, v26
	v_mul_f32_e32 v29, v34, v29
	v_mul_f32_e32 v28, v34, v28
	v_mul_f32_e32 v31, v34, v31
	v_mul_f32_e32 v30, v34, v30
	v_mul_f32_e32 v33, v34, v33
	v_mul_f32_e32 v32, v34, v32
	v_bfe_u32 v34, v0, 8, 2
	v_lshlrev_b32_e32 v34, 3, v34
	v_xor_b32_e32 v34, v34, v128
	v_lshlrev_b32_e32 v34, 1, v34
	v_mul_f32_e32 v29, v8, v29
	v_add3_u32 v34, s20, v34, v0
	v_cvt_pk_bf16_f32 v26, v26, s0
	v_mul_f32_e32 v28, v9, v28
	ds_write_b16 v34, v26 offset:272
	v_cvt_pk_bf16_f32 v26, v29, s0
	v_mul_f32_e32 v31, v2, v31
	ds_write_b16 v34, v26 offset:544
	v_cvt_pk_bf16_f32 v26, v28, s0
	v_mul_f32_e32 v30, v3, v30
	ds_write_b16 v34, v26 offset:816
	v_cvt_pk_bf16_f32 v26, v31, s0
	v_mul_f32_e32 v33, v4, v33
	ds_write_b16 v34, v26 offset:1088
	v_cvt_pk_bf16_f32 v26, v30, s0
	v_mul_f32_e32 v27, v6, v27
	v_mul_f32_e32 v32, v5, v32
	ds_write_b16 v34, v26 offset:1360
	v_cvt_pk_bf16_f32 v26, v33, s0
	v_cvt_pk_bf16_f32 v27, v27, s0
	ds_write_b16 v34, v26 offset:1632
	v_cvt_pk_bf16_f32 v26, v32, s0
	ds_write_b16 v34, v27
	ds_write_b16 v34, v26 offset:1904
	v_lshl_add_u32 v30, v87, 5, s7
	ds_read_b128 v[26:29], v30
	ds_read_b128 v[30:33], v30 offset:16
	s_waitcnt lgkmcnt(1)
	v_add_f32_e32 v26, v26, v27
	v_add_f32_e32 v27, v28, v29
	v_add_f32_e32 v26, v26, v27
	s_waitcnt lgkmcnt(0)
	v_add_f32_e32 v27, v30, v31
	v_add_f32_e32 v26, v26, v27
	v_add_f32_e32 v27, v32, v33
	v_add_f32_e32 v26, v27, v26
	v_fmamk_f32 v26, v26, 0x3b000000, v235
	v_rsq_f32_e32 v26, v26
	s_nop 0
	v_mul_f32_e32 v18, v26, v18
	v_mul_f32_e32 v19, v26, v19
	v_mul_f32_e32 v18, v7, v18
	v_mul_f32_e32 v21, v26, v21
	v_mul_f32_e32 v20, v26, v20
	v_mul_f32_e32 v23, v26, v23
	v_mul_f32_e32 v22, v26, v22
	v_mul_f32_e32 v25, v26, v25
	v_mul_f32_e32 v24, v26, v24
	v_bfe_u32 v26, v0, 8, 2
	v_lshlrev_b32_e32 v26, 3, v26
	v_xor_b32_e32 v26, v26, v87
	v_lshlrev_b32_e32 v26, 1, v26
	v_mul_f32_e32 v21, v8, v21
	v_add3_u32 v26, s20, v26, v0
	v_cvt_pk_bf16_f32 v18, v18, s0
	v_mul_f32_e32 v20, v9, v20
	ds_write_b16 v26, v18 offset:272
	v_cvt_pk_bf16_f32 v18, v21, s0
	v_mul_f32_e32 v23, v2, v23
	ds_write_b16 v26, v18 offset:544
	v_cvt_pk_bf16_f32 v18, v20, s0
	v_mul_f32_e32 v22, v3, v22
	ds_write_b16 v26, v18 offset:816
	v_cvt_pk_bf16_f32 v18, v23, s0
	v_mul_f32_e32 v25, v4, v25
	ds_write_b16 v26, v18 offset:1088
	v_cvt_pk_bf16_f32 v18, v22, s0
	v_mul_f32_e32 v19, v6, v19
	v_mul_f32_e32 v24, v5, v24
	ds_write_b16 v26, v18 offset:1360
	v_cvt_pk_bf16_f32 v18, v25, s0
	v_cvt_pk_bf16_f32 v19, v19, s0
	ds_write_b16 v26, v18 offset:1632
	v_cvt_pk_bf16_f32 v18, v24, s0
	ds_write_b16 v26, v19
	ds_write_b16 v26, v18 offset:1904
	v_lshl_add_u32 v22, v49, 5, s7
	ds_read_b128 v[18:21], v22
	ds_read_b128 v[22:25], v22 offset:16
	s_waitcnt lgkmcnt(1)
	v_add_f32_e32 v18, v18, v19
	v_add_f32_e32 v19, v20, v21
	v_add_f32_e32 v18, v18, v19
	s_waitcnt lgkmcnt(0)
	v_add_f32_e32 v19, v22, v23
	v_add_f32_e32 v18, v18, v19
	v_add_f32_e32 v19, v24, v25
	v_add_f32_e32 v18, v19, v18
	v_fmamk_f32 v18, v18, 0x3b000000, v235
	v_rsq_f32_e32 v18, v18
	s_nop 0
	v_mul_f32_e32 v10, v18, v10
	v_mul_f32_e32 v7, v7, v10
	v_mul_f32_e32 v10, v18, v13
	v_mul_f32_e32 v8, v8, v10
	v_mul_f32_e32 v10, v18, v12
	v_mul_f32_e32 v9, v9, v10
	v_mul_f32_e32 v10, v18, v15
	v_mul_f32_e32 v2, v2, v10
	v_mul_f32_e32 v10, v18, v14
	v_mul_f32_e32 v3, v3, v10
	v_mul_f32_e32 v10, v18, v17
	v_mul_f32_e32 v11, v18, v11
	v_mul_f32_e32 v4, v4, v10
	v_mul_f32_e32 v10, v18, v16
	v_mul_f32_e32 v6, v6, v11
	v_mul_f32_e32 v5, v5, v10
	v_bfe_u32 v10, v0, 8, 2
	v_lshlrev_b32_e32 v10, 3, v10
	v_xor_b32_e32 v10, v10, v49
	v_lshlrev_b32_e32 v10, 1, v10
	v_cvt_pk_bf16_f32 v6, v6, s0
	v_add3_u32 v0, s20, v10, v0
	v_cvt_pk_bf16_f32 v2, v2, s0
	ds_write_b16 v0, v6
	v_cvt_pk_bf16_f32 v6, v7, s0
	ds_write_b16 v0, v2 offset:1088
	v_cvt_pk_bf16_f32 v2, v3, s0
	ds_write_b16 v0, v6 offset:272
	v_cvt_pk_bf16_f32 v6, v8, s0
	ds_write_b16 v0, v2 offset:1360
	v_cvt_pk_bf16_f32 v2, v4, s0
	ds_write_b16 v0, v6 offset:544
	v_cvt_pk_bf16_f32 v6, v9, s0
	ds_write_b16 v0, v2 offset:1632
	v_cvt_pk_bf16_f32 v2, v5, s0
	ds_write_b16 v0, v6 offset:816
	ds_write_b16 v0, v2 offset:1904
	v_lshlrev_b32_e32 v0, 4, v106
	v_lshlrev_b32_e32 v4, 2, v106
	v_lshl_add_u64 v[2:3], s[4:5], 0, v[0:1]
	v_lshl_or_b32 v54, s12, 7, v4
	v_lshlrev_b32_e32 v4, 8, v105
	v_mov_b32_e32 v5, v1
	v_lshl_add_u64 v[82:83], v[2:3], 0, v[4:5]
	s_mov_b64 s[4:5], 0x1620000
	v_lshl_add_u64 v[6:7], v[82:83], 0, s[4:5]
	s_mov_b32 s4, 0x1620000
	v_add_co_u32_e32 v2, vcc, s4, v82
	s_waitcnt lgkmcnt(0)
	s_nop 0
	v_addc_co_u32_e32 v3, vcc, 0, v83, vcc
	s_barrier
	global_load_dwordx4 v[2:5], v[2:3], off
	s_nop 0
	global_load_dwordx4 v[50:53], v[6:7], off offset:32
	v_mul_u32_u24_e32 v8, 0x110, v105
	v_and_b32_e32 v42, 16, v105
	v_xor_b32_e32 v0, v42, v0
	v_add3_u32 v0, s20, v8, v0
	ds_read_b128 v[42:45], v0 offset:8736
	ds_read_b128 v[46:49], v0
	ds_read_b128 v[38:41], v0 offset:32
	s_waitcnt vmcnt(1) lgkmcnt(1)
	v_mfma_f32_32x32x16_bf16 v[18:33], v[2:5], v[46:49], 0
	ds_read_b128 v[34:37], v0 offset:8704
	v_ashrrev_i32_e32 v55, 31, v54
	v_lshl_add_u64 v[98:99], v[54:55], 2, s[16:17]
	s_mov_b32 s4, 0x1622000
	v_mfma_f32_32x32x16_bf16 v[2:17], v[2:5], v[42:45], 0
	s_waitcnt vmcnt(0) lgkmcnt(1)
	v_mfma_f32_32x32x16_bf16 v[18:33], v[50:53], v[38:41], v[18:33]
	s_waitcnt lgkmcnt(0)
	v_mfma_f32_32x32x16_bf16 v[2:17], v[50:53], v[34:37], v[2:17]
	global_load_dwordx4 v[50:53], v[98:99], off
	global_load_dwordx4 v[54:57], v[98:99], off offset:32
	global_load_dwordx4 v[58:61], v[98:99], off offset:64
	global_load_dwordx4 v[62:65], v[98:99], off offset:96
	s_nop 5
	v_mov_b32_e32 v66, v18
	s_nop 0
	v_mov_b32_e32 v67, v2
	v_mov_b32_e32 v2, v19
	s_waitcnt vmcnt(3)
	v_pk_add_f32 v[2:3], v[2:3], v[50:51] op_sel:[0,1]
	s_nop 0
	v_cvt_pk_bf16_f32 v108, v2, v3
	v_mov_b32_e32 v2, v20
	v_mov_b32_e32 v3, v4
	v_pk_add_f32 v[2:3], v[2:3], v[52:53] op_sel_hi:[1,0]
	v_mov_b32_e32 v4, v21
	v_cvt_pk_bf16_f32 v109, v2, v3
	v_mov_b32_e32 v2, v53
	v_pk_add_f32 v[2:3], v[4:5], v[2:3] op_sel_hi:[1,0]
	v_pk_add_f32 v[66:67], v[66:67], v[50:51] op_sel_hi:[1,0]
	v_cvt_pk_bf16_f32 v110, v2, v3
	v_mov_b32_e32 v2, v22
	v_mov_b32_e32 v3, v6
	s_waitcnt vmcnt(2)
	v_pk_add_f32 v[2:3], v[2:3], v[54:55] op_sel_hi:[1,0]
	v_mov_b32_e32 v6, v23
	v_cvt_pk_bf16_f32 v111, v2, v3
	v_pk_add_f32 v[2:3], v[6:7], v[54:55] op_sel:[0,1]
	v_add_co_u32_e32 v6, vcc, s4, v82
	v_cvt_pk_bf16_f32 v112, v2, v3
	v_mov_b32_e32 v2, v24
	v_mov_b32_e32 v3, v8
	v_pk_add_f32 v[2:3], v[2:3], v[56:57] op_sel_hi:[1,0]
	v_mov_b32_e32 v8, v25
	v_cvt_pk_bf16_f32 v113, v2, v3
	v_mov_b32_e32 v2, v57
	v_pk_add_f32 v[2:3], v[8:9], v[2:3] op_sel_hi:[1,0]
	v_addc_co_u32_e32 v7, vcc, 0, v83, vcc
	v_cvt_pk_bf16_f32 v114, v2, v3
	v_mov_b32_e32 v2, v26
	v_mov_b32_e32 v3, v10
	s_waitcnt vmcnt(1)
	v_pk_add_f32 v[2:3], v[2:3], v[58:59] op_sel_hi:[1,0]
	v_mov_b32_e32 v10, v27
	v_cvt_pk_bf16_f32 v115, v2, v3
	v_pk_add_f32 v[2:3], v[10:11], v[58:59] op_sel:[0,1]
	v_cvt_pk_bf16_f32 v107, v66, v67
	v_cvt_pk_bf16_f32 v116, v2, v3
	v_mov_b32_e32 v2, v28
	v_mov_b32_e32 v3, v12
	v_pk_add_f32 v[2:3], v[2:3], v[60:61] op_sel_hi:[1,0]
	v_mov_b32_e32 v12, v29
	v_cvt_pk_bf16_f32 v117, v2, v3
	v_mov_b32_e32 v2, v61
	v_pk_add_f32 v[2:3], v[12:13], v[2:3] op_sel_hi:[1,0]
	s_mov_b32 s4, 0x1624000
	v_cvt_pk_bf16_f32 v118, v2, v3
	v_mov_b32_e32 v2, v30
	v_mov_b32_e32 v3, v14
	s_waitcnt vmcnt(0)
	v_pk_add_f32 v[2:3], v[2:3], v[62:63] op_sel_hi:[1,0]
	v_mov_b32_e32 v14, v31
	v_cvt_pk_bf16_f32 v119, v2, v3
	v_pk_add_f32 v[2:3], v[14:15], v[62:63] op_sel:[0,1]
	s_nop 0
	v_cvt_pk_bf16_f32 v120, v2, v3
	v_mov_b32_e32 v2, v32
	v_mov_b32_e32 v3, v16
	v_pk_add_f32 v[2:3], v[2:3], v[64:65] op_sel_hi:[1,0]
	v_mov_b32_e32 v16, v33
	v_cvt_pk_bf16_f32 v121, v2, v3
	v_mov_b32_e32 v2, v65
	v_pk_add_f32 v[2:3], v[16:17], v[2:3] op_sel_hi:[1,0]
	s_nop 0
	v_cvt_pk_bf16_f32 v122, v2, v3
	global_load_dwordx4 v[2:5], v[6:7], off
	global_load_dwordx4 v[50:53], v[6:7], off offset:32
	global_load_dwordx4 v[54:57], v[6:7], off offset:64
	global_load_dwordx4 v[66:69], v[6:7], off offset:96
	s_waitcnt vmcnt(3)
	v_mfma_f32_32x32x16_bf16 v[18:33], v[2:5], v[46:49], 0
	ds_read_b128 v[62:65], v0 offset:64
	ds_read_b128 v[58:61], v0 offset:8800
	v_mfma_f32_32x32x16_bf16 v[2:17], v[2:5], v[42:45], 0
	s_waitcnt vmcnt(2)
	v_mfma_f32_32x32x16_bf16 v[18:33], v[50:53], v[38:41], v[18:33]
	v_mfma_f32_32x32x16_bf16 v[2:17], v[50:53], v[34:37], v[2:17]
	s_waitcnt vmcnt(1) lgkmcnt(1)
	v_mfma_f32_32x32x16_bf16 v[18:33], v[54:57], v[62:65], v[18:33]
	s_waitcnt lgkmcnt(0)
	v_mfma_f32_32x32x16_bf16 v[2:17], v[54:57], v[58:61], v[2:17]
	ds_read_b128 v[50:53], v0 offset:96
	ds_read_b128 v[54:57], v0 offset:8768
	s_waitcnt vmcnt(0) lgkmcnt(1)
	v_mfma_f32_32x32x16_bf16 v[18:33], v[66:69], v[50:53], v[18:33]
	s_waitcnt lgkmcnt(0)
	v_mfma_f32_32x32x16_bf16 v[2:17], v[66:69], v[54:57], v[2:17]
	global_load_dwordx4 v[66:69], v[98:99], off offset:128
	global_load_dwordx4 v[70:73], v[98:99], off offset:160
	global_load_dwordx4 v[74:77], v[98:99], off offset:192
	global_load_dwordx4 v[78:81], v[98:99], off offset:224
	s_nop 5
	v_mov_b32_e32 v84, v18
	s_nop 0
	v_mov_b32_e32 v85, v2
	v_mov_b32_e32 v2, v19
	s_waitcnt vmcnt(3)
	v_pk_add_f32 v[2:3], v[2:3], v[66:67] op_sel:[0,1]
	s_nop 0
	v_cvt_pk_bf16_f32 v124, v2, v3
	v_mov_b32_e32 v2, v20
	v_mov_b32_e32 v3, v4
	v_pk_add_f32 v[2:3], v[2:3], v[68:69] op_sel_hi:[1,0]
	v_mov_b32_e32 v4, v21
	v_cvt_pk_bf16_f32 v125, v2, v3
	v_mov_b32_e32 v2, v69
	v_pk_add_f32 v[2:3], v[4:5], v[2:3] op_sel_hi:[1,0]
	v_pk_add_f32 v[84:85], v[84:85], v[66:67] op_sel_hi:[1,0]
	v_cvt_pk_bf16_f32 v126, v2, v3
	v_mov_b32_e32 v2, v22
	v_mov_b32_e32 v3, v6
	s_waitcnt vmcnt(2)
	v_pk_add_f32 v[2:3], v[2:3], v[70:71] op_sel_hi:[1,0]
	v_mov_b32_e32 v6, v23
	v_cvt_pk_bf16_f32 v127, v2, v3
	v_pk_add_f32 v[2:3], v[6:7], v[70:71] op_sel:[0,1]
	v_cvt_pk_bf16_f32 v123, v84, v85
	v_cvt_pk_bf16_f32 v128, v2, v3
	v_mov_b32_e32 v2, v24
	v_mov_b32_e32 v3, v8
	v_pk_add_f32 v[2:3], v[2:3], v[72:73] op_sel_hi:[1,0]
	v_mov_b32_e32 v8, v25
	v_cvt_pk_bf16_f32 v129, v2, v3
	v_mov_b32_e32 v2, v73
	v_pk_add_f32 v[2:3], v[8:9], v[2:3] op_sel_hi:[1,0]
	s_nop 0
	v_cvt_pk_bf16_f32 v130, v2, v3
	v_mov_b32_e32 v2, v26
	v_mov_b32_e32 v3, v10
	s_waitcnt vmcnt(1)
	v_pk_add_f32 v[2:3], v[2:3], v[74:75] op_sel_hi:[1,0]
	v_mov_b32_e32 v10, v27
	v_cvt_pk_bf16_f32 v131, v2, v3
	v_pk_add_f32 v[2:3], v[10:11], v[74:75] op_sel:[0,1]
	s_nop 0
	v_cvt_pk_bf16_f32 v132, v2, v3
	v_mov_b32_e32 v2, v28
	v_mov_b32_e32 v3, v12
	v_pk_add_f32 v[2:3], v[2:3], v[76:77] op_sel_hi:[1,0]
	v_mov_b32_e32 v12, v29
	v_cvt_pk_bf16_f32 v133, v2, v3
	v_mov_b32_e32 v2, v77
	v_pk_add_f32 v[2:3], v[12:13], v[2:3] op_sel_hi:[1,0]
	s_nop 0
	v_cvt_pk_bf16_f32 v134, v2, v3
	v_mov_b32_e32 v2, v30
	v_mov_b32_e32 v3, v14
	s_waitcnt vmcnt(0)
	v_pk_add_f32 v[2:3], v[2:3], v[78:79] op_sel_hi:[1,0]
	v_mov_b32_e32 v14, v31
	v_cvt_pk_bf16_f32 v135, v2, v3
	v_pk_add_f32 v[2:3], v[14:15], v[78:79] op_sel:[0,1]
	s_nop 0
	v_cvt_pk_bf16_f32 v136, v2, v3
	v_mov_b32_e32 v2, v32
	v_mov_b32_e32 v3, v16
	v_pk_add_f32 v[2:3], v[2:3], v[80:81] op_sel_hi:[1,0]
	v_mov_b32_e32 v16, v33
	v_cvt_pk_bf16_f32 v137, v2, v3
	v_mov_b32_e32 v2, v81
	v_pk_add_f32 v[2:3], v[16:17], v[2:3] op_sel_hi:[1,0]
	s_nop 0
	v_cvt_pk_bf16_f32 v138, v2, v3
	v_add_co_u32_e32 v2, vcc, s4, v82
	s_mov_b32 s4, 0x1626000
	s_nop 0
	v_addc_co_u32_e32 v3, vcc, 0, v83, vcc
	global_load_dwordx4 v[18:21], v[2:3], off
	global_load_dwordx4 v[66:69], v[2:3], off offset:32
	global_load_dwordx4 v[70:73], v[2:3], off offset:64
	global_load_dwordx4 v[74:77], v[2:3], off offset:96
	global_load_dwordx4 v[78:81], v[2:3], off offset:128
	global_load_dwordx4 v[84:87], v[2:3], off offset:160
	s_waitcnt vmcnt(5)
	v_mfma_f32_32x32x16_bf16 v[2:17], v[18:21], v[46:49], 0
	v_mfma_f32_32x32x16_bf16 v[18:33], v[18:21], v[42:45], 0
	s_waitcnt vmcnt(4)
	v_mfma_f32_32x32x16_bf16 v[2:17], v[66:69], v[38:41], v[2:17]
	v_mfma_f32_32x32x16_bf16 v[18:33], v[66:69], v[34:37], v[18:33]
	s_waitcnt vmcnt(3)
	v_mfma_f32_32x32x16_bf16 v[2:17], v[70:73], v[62:65], v[2:17]
	v_mfma_f32_32x32x16_bf16 v[18:33], v[70:73], v[58:61], v[18:33]
	ds_read_b128 v[66:69], v0 offset:128
	ds_read_b128 v[70:73], v0 offset:8864
	s_waitcnt vmcnt(2)
	v_mfma_f32_32x32x16_bf16 v[2:17], v[74:77], v[50:53], v[2:17]
	v_mfma_f32_32x32x16_bf16 v[18:33], v[74:77], v[54:57], v[18:33]
	s_waitcnt vmcnt(1) lgkmcnt(1)
	v_mfma_f32_32x32x16_bf16 v[2:17], v[78:81], v[66:69], v[2:17]
	s_waitcnt lgkmcnt(0)
	v_mfma_f32_32x32x16_bf16 v[18:33], v[78:81], v[70:73], v[18:33]
	ds_read_b128 v[74:77], v0 offset:160
	ds_read_b128 v[78:81], v0 offset:8832
	s_waitcnt vmcnt(0) lgkmcnt(1)
	v_mfma_f32_32x32x16_bf16 v[2:17], v[84:87], v[74:77], v[2:17]
	s_waitcnt lgkmcnt(0)
	v_mfma_f32_32x32x16_bf16 v[18:33], v[84:87], v[78:81], v[18:33]
	global_load_dwordx4 v[84:87], v[98:99], off offset:256
	global_load_dwordx4 v[88:91], v[98:99], off offset:288
	global_load_dwordx4 v[92:95], v[98:99], off offset:320
	global_load_dwordx4 v[156:159], v[98:99], off offset:352
	s_nop 5
	v_mov_b32_e32 v96, v2
	s_nop 0
	v_mov_b32_e32 v97, v18
	v_mov_b32_e32 v18, v3
	s_waitcnt vmcnt(3)
	v_pk_add_f32 v[2:3], v[18:19], v[84:85] op_sel:[0,1]
	s_nop 0
	v_cvt_pk_bf16_f32 v150, v2, v3
	v_mov_b32_e32 v2, v4
	v_mov_b32_e32 v3, v20
	v_pk_add_f32 v[2:3], v[2:3], v[86:87] op_sel_hi:[1,0]
	v_mov_b32_e32 v20, v5
	v_cvt_pk_bf16_f32 v151, v2, v3
	v_mov_b32_e32 v2, v87
	v_pk_add_f32 v[2:3], v[20:21], v[2:3] op_sel_hi:[1,0]
	v_pk_add_f32 v[96:97], v[96:97], v[84:85] op_sel_hi:[1,0]
	v_cvt_pk_bf16_f32 v152, v2, v3
	v_mov_b32_e32 v2, v6
	v_mov_b32_e32 v3, v22
	s_waitcnt vmcnt(2)
	v_pk_add_f32 v[2:3], v[2:3], v[88:89] op_sel_hi:[1,0]
	v_mov_b32_e32 v22, v7
	v_cvt_pk_bf16_f32 v153, v2, v3
	v_pk_add_f32 v[2:3], v[22:23], v[88:89] op_sel:[0,1]
	v_cvt_pk_bf16_f32 v154, v96, v97
	v_cvt_pk_bf16_f32 v146, v2, v3
	v_mov_b32_e32 v2, v8
	v_mov_b32_e32 v3, v24
	v_pk_add_f32 v[2:3], v[2:3], v[90:91] op_sel_hi:[1,0]
	v_mov_b32_e32 v24, v9
	v_cvt_pk_bf16_f32 v147, v2, v3
	v_mov_b32_e32 v2, v91
	v_pk_add_f32 v[2:3], v[24:25], v[2:3] op_sel_hi:[1,0]
	s_nop 0
	v_cvt_pk_bf16_f32 v148, v2, v3
	v_mov_b32_e32 v2, v10
	v_mov_b32_e32 v3, v26
	s_waitcnt vmcnt(1)
	v_pk_add_f32 v[2:3], v[2:3], v[92:93] op_sel_hi:[1,0]
	v_mov_b32_e32 v26, v11
	v_cvt_pk_bf16_f32 v149, v2, v3
	v_pk_add_f32 v[2:3], v[26:27], v[92:93] op_sel:[0,1]
	s_nop 0
	v_cvt_pk_bf16_f32 v142, v2, v3
	v_mov_b32_e32 v2, v12
	v_mov_b32_e32 v3, v28
	v_pk_add_f32 v[2:3], v[2:3], v[94:95] op_sel_hi:[1,0]
	v_mov_b32_e32 v28, v13
	v_cvt_pk_bf16_f32 v143, v2, v3
	v_mov_b32_e32 v2, v95
	v_pk_add_f32 v[2:3], v[28:29], v[2:3] op_sel_hi:[1,0]
	s_nop 0
	v_cvt_pk_bf16_f32 v144, v2, v3
	v_mov_b32_e32 v2, v14
	v_mov_b32_e32 v3, v30
	s_waitcnt vmcnt(0)
	v_pk_add_f32 v[2:3], v[2:3], v[156:157] op_sel_hi:[1,0]
	v_mov_b32_e32 v30, v15
	v_cvt_pk_bf16_f32 v145, v2, v3
	v_pk_add_f32 v[2:3], v[30:31], v[156:157] op_sel:[0,1]
	s_nop 0
	v_cvt_pk_bf16_f32 v139, v2, v3
	v_mov_b32_e32 v2, v16
	v_mov_b32_e32 v3, v32
	v_pk_add_f32 v[2:3], v[2:3], v[158:159] op_sel_hi:[1,0]
	v_mov_b32_e32 v32, v17
	v_cvt_pk_bf16_f32 v140, v2, v3
	v_mov_b32_e32 v2, v159
	v_pk_add_f32 v[2:3], v[32:33], v[2:3] op_sel_hi:[1,0]
	s_nop 0
	v_cvt_pk_bf16_f32 v141, v2, v3
	v_add_co_u32_e32 v2, vcc, s4, v82
	s_ashr_i32 s4, s23, 31
	s_nop 0
	v_addc_co_u32_e32 v3, vcc, 0, v83, vcc
	global_load_dwordx4 v[18:21], v[2:3], off
	global_load_dwordx4 v[82:85], v[2:3], off offset:32
	global_load_dwordx4 v[86:89], v[2:3], off offset:64
	global_load_dwordx4 v[90:93], v[2:3], off offset:96
	global_load_dwordx4 v[94:97], v[2:3], off offset:128
	global_load_dwordx4 v[156:159], v[2:3], off offset:160
	global_load_dwordx4 v[160:163], v[2:3], off offset:192
	global_load_dwordx4 v[164:167], v[2:3], off offset:224
	s_waitcnt vmcnt(7)
	v_mfma_f32_32x32x16_bf16 v[2:17], v[18:21], v[46:49], 0
	s_add_u32 s20, s8, s23
	s_addc_u32 s21, s9, s4
	s_add_u32 s16, s20, 0xffffff88
	s_addc_u32 s17, s21, -1
	s_lshl_b64 s[4:5], s[16:17], 11
	v_mfma_f32_32x32x16_bf16 v[18:33], v[18:21], v[42:45], 0
	s_waitcnt vmcnt(6)
	v_mfma_f32_32x32x16_bf16 v[2:17], v[82:85], v[38:41], v[2:17]
	v_mfma_f32_32x32x16_bf16 v[18:33], v[82:85], v[34:37], v[18:33]
	ds_read_b128 v[34:37], v0 offset:192
	ds_read_b128 v[38:41], v0 offset:8928
	v_or_b32_e32 v82, s6, v105
	v_lshlrev_b32_e32 v82, 1, v82
	v_mul_u32_u24_e32 v83, 0x1040, v106
	v_add3_u32 v82, 0, v82, v83
	v_add_u32_e32 v83, 0x10400, v82
	v_cmp_eq_u32_e64 s[6:7], 0, v103
	s_waitcnt vmcnt(5)
	v_mfma_f32_32x32x16_bf16 v[2:17], v[86:89], v[62:65], v[2:17]
	v_mfma_f32_32x32x16_bf16 v[18:33], v[86:89], v[58:61], v[18:33]
	s_waitcnt vmcnt(4)
	v_mfma_f32_32x32x16_bf16 v[2:17], v[90:93], v[50:53], v[2:17]
	v_mfma_f32_32x32x16_bf16 v[18:33], v[90:93], v[54:57], v[18:33]
	s_waitcnt vmcnt(3)
	v_mfma_f32_32x32x16_bf16 v[2:17], v[94:97], v[66:69], v[2:17]
	v_mfma_f32_32x32x16_bf16 v[18:33], v[94:97], v[70:73], v[18:33]
	s_waitcnt vmcnt(2)
	v_mfma_f32_32x32x16_bf16 v[2:17], v[156:159], v[74:77], v[2:17]
	v_mfma_f32_32x32x16_bf16 v[18:33], v[156:159], v[78:81], v[18:33]
	s_waitcnt vmcnt(1) lgkmcnt(1)
	v_mfma_f32_32x32x16_bf16 v[2:17], v[160:163], v[34:37], v[2:17]
	s_waitcnt lgkmcnt(0)
	v_mfma_f32_32x32x16_bf16 v[18:33], v[160:163], v[38:41], v[18:33]
	ds_read_b128 v[34:37], v0 offset:224
	ds_read_b128 v[38:41], v0 offset:8896
	s_waitcnt vmcnt(0) lgkmcnt(1)
	v_mfma_f32_32x32x16_bf16 v[2:17], v[164:167], v[34:37], v[2:17]
	s_waitcnt lgkmcnt(0)
	v_mfma_f32_32x32x16_bf16 v[18:33], v[164:167], v[38:41], v[18:33]
	global_load_dwordx4 v[34:37], v[98:99], off offset:384
	global_load_dwordx4 v[38:41], v[98:99], off offset:416
	global_load_dwordx4 v[42:45], v[98:99], off offset:448
	global_load_dwordx4 v[46:49], v[98:99], off offset:480
	s_nop 5
	v_mov_b32_e32 v50, v2
	s_nop 0
	v_mov_b32_e32 v51, v18
	v_mov_b32_e32 v18, v3
	s_waitcnt vmcnt(3)
	v_pk_add_f32 v[2:3], v[18:19], v[34:35] op_sel:[0,1]
	s_nop 0
	v_cvt_pk_bf16_f32 v67, v2, v3
	v_mov_b32_e32 v2, v4
	v_mov_b32_e32 v3, v20
	v_pk_add_f32 v[2:3], v[2:3], v[36:37] op_sel_hi:[1,0]
	v_mov_b32_e32 v20, v5
	v_mov_b32_e32 v0, v37
	v_cvt_pk_bf16_f32 v68, v2, v3
	v_pk_add_f32 v[2:3], v[20:21], v[0:1] op_sel_hi:[1,0]
	s_waitcnt vmcnt(2)
	v_mov_b32_e32 v0, v41
	v_cvt_pk_bf16_f32 v69, v2, v3
	v_mov_b32_e32 v2, v6
	v_mov_b32_e32 v3, v22
	v_pk_add_f32 v[2:3], v[2:3], v[38:39] op_sel_hi:[1,0]
	v_mov_b32_e32 v22, v7
	v_cvt_pk_bf16_f32 v70, v2, v3
	v_pk_add_f32 v[2:3], v[22:23], v[38:39] op_sel:[0,1]
	v_pk_add_f32 v[50:51], v[50:51], v[34:35] op_sel_hi:[1,0]
	v_cvt_pk_bf16_f32 v71, v2, v3
	v_mov_b32_e32 v2, v8
	v_mov_b32_e32 v3, v24
	v_pk_add_f32 v[2:3], v[2:3], v[40:41] op_sel_hi:[1,0]
	v_mov_b32_e32 v24, v9
	v_cvt_pk_bf16_f32 v72, v2, v3
	v_pk_add_f32 v[2:3], v[24:25], v[0:1] op_sel_hi:[1,0]
	s_waitcnt vmcnt(1)
	v_mov_b32_e32 v0, v45
	v_cvt_pk_bf16_f32 v73, v2, v3
	v_mov_b32_e32 v2, v10
	v_mov_b32_e32 v3, v26
	v_pk_add_f32 v[2:3], v[2:3], v[42:43] op_sel_hi:[1,0]
	v_mov_b32_e32 v26, v11
	v_cvt_pk_bf16_f32 v74, v2, v3
	v_pk_add_f32 v[2:3], v[26:27], v[42:43] op_sel:[0,1]
	v_cvt_pk_bf16_f32 v66, v50, v51
	v_cvt_pk_bf16_f32 v75, v2, v3
	v_mov_b32_e32 v2, v12
	v_mov_b32_e32 v3, v28
	v_pk_add_f32 v[2:3], v[2:3], v[44:45] op_sel_hi:[1,0]
	v_mov_b32_e32 v28, v13
	v_cvt_pk_bf16_f32 v76, v2, v3
	v_pk_add_f32 v[2:3], v[28:29], v[0:1] op_sel_hi:[1,0]
	s_waitcnt vmcnt(0)
	v_mov_b32_e32 v0, v49
	v_cvt_pk_bf16_f32 v77, v2, v3
	v_mov_b32_e32 v2, v14
	v_mov_b32_e32 v3, v30
	v_pk_add_f32 v[2:3], v[2:3], v[46:47] op_sel_hi:[1,0]
	v_mov_b32_e32 v30, v15
	v_cvt_pk_bf16_f32 v78, v2, v3
	v_pk_add_f32 v[2:3], v[30:31], v[46:47] op_sel:[0,1]
	s_nop 0
	v_cvt_pk_bf16_f32 v79, v2, v3
	v_mov_b32_e32 v2, v16
	v_mov_b32_e32 v3, v32
	v_pk_add_f32 v[2:3], v[2:3], v[48:49] op_sel_hi:[1,0]
	v_mov_b32_e32 v32, v17
	v_cvt_pk_bf16_f32 v80, v2, v3
	v_pk_add_f32 v[2:3], v[32:33], v[0:1] op_sel_hi:[1,0]
	v_lshlrev_b32_e32 v0, 4, v103
	v_cvt_pk_bf16_f32 v81, v2, v3
	v_lshl_add_u64 v[2:3], s[14:15], 0, v[0:1]
	v_lshl_add_u64 v[2:3], v[2:3], 0, s[4:5]
	v_add_co_u32_e32 v4, vcc, s74, v2
	s_movk_i32 s4, 0x2000
	s_nop 0
	v_addc_co_u32_e32 v5, vcc, 0, v3, vcc
	v_add_co_u32_e32 v6, vcc, s4, v2
	global_load_dwordx4 v[62:65], v[2:3], off
	global_load_dwordx4 v[58:61], v[2:3], off offset:2048
	v_addc_co_u32_e32 v7, vcc, 0, v3, vcc
	s_movk_i32 s4, 0x3000
	global_load_dwordx4 v[54:57], v[6:7], off offset:-4096
	global_load_dwordx4 v[50:53], v[4:5], off offset:2048
	global_load_dwordx4 v[46:49], v[6:7], off
	global_load_dwordx4 v[42:45], v[6:7], off offset:2048
	v_add_co_u32_e32 v4, vcc, s4, v2
	s_movk_i32 s4, 0x4000
	s_nop 0
	v_addc_co_u32_e32 v5, vcc, 0, v3, vcc
	v_add_co_u32_e32 v6, vcc, s4, v2
	s_movk_i32 s4, 0x5000
	s_nop 0
	v_addc_co_u32_e32 v7, vcc, 0, v3, vcc
	global_load_dwordx4 v[38:41], v[6:7], off offset:-4096
	global_load_dwordx4 v[34:37], v[4:5], off offset:2048
	global_load_dwordx4 v[30:33], v[6:7], off
	global_load_dwordx4 v[26:29], v[6:7], off offset:2048
	v_add_co_u32_e32 v4, vcc, s4, v2
	s_movk_i32 s4, 0x6000
	s_nop 0
	v_addc_co_u32_e32 v5, vcc, 0, v3, vcc
	v_add_co_u32_e32 v6, vcc, s4, v2
	s_movk_i32 s4, 0x7000
	s_nop 0
	v_addc_co_u32_e32 v7, vcc, 0, v3, vcc
	v_add_co_u32_e32 v2, vcc, s4, v2
	global_load_dwordx4 v[22:25], v[6:7], off offset:-4096
	global_load_dwordx4 v[18:21], v[4:5], off offset:2048
	global_load_dwordx4 v[14:17], v[6:7], off
	global_load_dwordx4 v[10:13], v[6:7], off offset:2048
	v_addc_co_u32_e32 v3, vcc, 0, v3, vcc
	global_load_dwordx4 v[6:9], v[2:3], off
	s_nop 0
	global_load_dwordx4 v[2:5], v[2:3], off offset:2048
	s_barrier
	ds_write_b16 v82, v107
	ds_write_b16_d16_hi v82, v107 offset:64
	ds_write_b16 v82, v108 offset:1040
	ds_write_b16_d16_hi v82, v108 offset:1104
	ds_write_b16 v82, v109 offset:2080
	ds_write_b16_d16_hi v82, v109 offset:2144
	ds_write_b16 v82, v110 offset:3120
	ds_write_b16_d16_hi v82, v110 offset:3184
	ds_write_b16 v82, v111 offset:8320
	ds_write_b16_d16_hi v82, v111 offset:8384
	ds_write_b16 v82, v112 offset:9360
	ds_write_b16_d16_hi v82, v112 offset:9424
	ds_write_b16 v82, v113 offset:10400
	ds_write_b16_d16_hi v82, v113 offset:10464
	ds_write_b16 v82, v114 offset:11440
	ds_write_b16_d16_hi v82, v114 offset:11504
	ds_write_b16 v82, v115 offset:16640
	ds_write_b16_d16_hi v82, v115 offset:16704
	ds_write_b16 v82, v116 offset:17680
	ds_write_b16_d16_hi v82, v116 offset:17744
	ds_write_b16 v82, v117 offset:18720
	ds_write_b16_d16_hi v82, v117 offset:18784
	ds_write_b16 v82, v118 offset:19760
	ds_write_b16_d16_hi v82, v118 offset:19824
	ds_write_b16 v82, v119 offset:24960
	ds_write_b16_d16_hi v82, v119 offset:25024
	ds_write_b16 v82, v120 offset:26000
	ds_write_b16_d16_hi v82, v120 offset:26064
	ds_write_b16 v82, v121 offset:27040
	ds_write_b16_d16_hi v82, v121 offset:27104
	ds_write_b16 v82, v122 offset:28080
	ds_write_b16_d16_hi v82, v122 offset:28144
	ds_write_b16 v82, v123 offset:33280
	ds_write_b16_d16_hi v82, v123 offset:33344
	ds_write_b16 v82, v124 offset:34320
	ds_write_b16_d16_hi v82, v124 offset:34384
	ds_write_b16 v82, v125 offset:35360
	ds_write_b16_d16_hi v82, v125 offset:35424
	ds_write_b16 v82, v126 offset:36400
	ds_write_b16_d16_hi v82, v126 offset:36464
	ds_write_b16 v82, v127 offset:41600
	ds_write_b16_d16_hi v82, v127 offset:41664
	ds_write_b16 v82, v128 offset:42640
	ds_write_b16_d16_hi v82, v128 offset:42704
	ds_write_b16 v82, v129 offset:43680
	ds_write_b16_d16_hi v82, v129 offset:43744
	ds_write_b16 v82, v130 offset:44720
	ds_write_b16_d16_hi v82, v130 offset:44784
	ds_write_b16 v82, v131 offset:49920
	ds_write_b16_d16_hi v82, v131 offset:49984
	ds_write_b16 v82, v132 offset:50960
	ds_write_b16_d16_hi v82, v132 offset:51024
	ds_write_b16 v82, v133 offset:52000
	ds_write_b16_d16_hi v82, v133 offset:52064
	ds_write_b16 v82, v134 offset:53040
	ds_write_b16_d16_hi v82, v134 offset:53104
	ds_write_b16 v82, v135 offset:58240
	ds_write_b16_d16_hi v82, v135 offset:58304
	ds_write_b16 v82, v136 offset:59280
	ds_write_b16_d16_hi v82, v136 offset:59344
	ds_write_b16 v82, v137 offset:60320
	ds_write_b16_d16_hi v82, v137 offset:60384
	ds_write_b16 v82, v138 offset:61360
	ds_write_b16_d16_hi v82, v138 offset:61424
	ds_write_b16 v83, v154
	v_add_u32_e32 v83, 0x10440, v82
	ds_write_b16_d16_hi v83, v154
	v_add_u32_e32 v83, 0x10810, v82
	ds_write_b16 v83, v150
	v_add_u32_e32 v83, 0x10850, v82
	ds_write_b16_d16_hi v83, v150
	v_add_u32_e32 v83, 0x10c20, v82
	ds_write_b16 v83, v151
	v_add_u32_e32 v83, 0x10c60, v82
	ds_write_b16_d16_hi v83, v151
	v_add_u32_e32 v83, 0x11030, v82
	ds_write_b16 v83, v152
	v_add_u32_e32 v83, 0x11070, v82
	ds_write_b16_d16_hi v83, v152
	v_add_u32_e32 v83, 0x12480, v82
	ds_write_b16 v83, v153
	v_add_u32_e32 v83, 0x124c0, v82
	ds_write_b16_d16_hi v83, v153
	v_add_u32_e32 v83, 0x12890, v82
	ds_write_b16 v83, v146
	v_add_u32_e32 v83, 0x128d0, v82
	ds_write_b16_d16_hi v83, v146
	v_add_u32_e32 v83, 0x12ca0, v82
	ds_write_b16 v83, v147
	v_add_u32_e32 v83, 0x12ce0, v82
	ds_write_b16_d16_hi v83, v147
	v_add_u32_e32 v83, 0x130b0, v82
	ds_write_b16 v83, v148
	v_add_u32_e32 v83, 0x130f0, v82
	ds_write_b16_d16_hi v83, v148
	v_add_u32_e32 v83, 0x14500, v82
	ds_write_b16 v83, v149
	v_add_u32_e32 v83, 0x14540, v82
	ds_write_b16_d16_hi v83, v149
	v_add_u32_e32 v83, 0x14910, v82
	ds_write_b16 v83, v142
	v_add_u32_e32 v83, 0x14950, v82
	ds_write_b16_d16_hi v83, v142
	v_add_u32_e32 v83, 0x14d20, v82
	ds_write_b16 v83, v143
	v_add_u32_e32 v83, 0x14d60, v82
	ds_write_b16_d16_hi v83, v143
	v_add_u32_e32 v83, 0x15130, v82
	ds_write_b16 v83, v144
	v_add_u32_e32 v83, 0x15170, v82
	ds_write_b16_d16_hi v83, v144
	v_add_u32_e32 v83, 0x16580, v82
	ds_write_b16 v83, v145
	v_add_u32_e32 v83, 0x165c0, v82
	ds_write_b16_d16_hi v83, v145
	v_add_u32_e32 v83, 0x16990, v82
	ds_write_b16 v83, v139
	v_add_u32_e32 v83, 0x169d0, v82
	ds_write_b16_d16_hi v83, v139
	v_add_u32_e32 v83, 0x16da0, v82
	ds_write_b16 v83, v140
	v_add_u32_e32 v83, 0x16de0, v82
	ds_write_b16_d16_hi v83, v140
	v_add_u32_e32 v83, 0x171b0, v82
	ds_write_b16 v83, v141
	v_add_u32_e32 v83, 0x171f0, v82
	ds_write_b16_d16_hi v83, v141
	v_add_u32_e32 v83, 0x18600, v82
	ds_write_b16 v83, v66
	v_add_u32_e32 v83, 0x18640, v82
	ds_write_b16_d16_hi v83, v66
	v_add_u32_e32 v66, 0x18a10, v82
	ds_write_b16 v66, v67
	v_add_u32_e32 v66, 0x18a50, v82
	ds_write_b16_d16_hi v66, v67
	v_add_u32_e32 v66, 0x18e20, v82
	ds_write_b16 v66, v68
	v_add_u32_e32 v66, 0x18e60, v82
	ds_write_b16_d16_hi v66, v68
	v_add_u32_e32 v66, 0x19230, v82
	ds_write_b16 v66, v69
	v_add_u32_e32 v66, 0x19270, v82
	ds_write_b16_d16_hi v66, v69
	v_add_u32_e32 v66, 0x1a680, v82
	ds_write_b16 v66, v70
	v_add_u32_e32 v66, 0x1a6c0, v82
	ds_write_b16_d16_hi v66, v70
	v_add_u32_e32 v66, 0x1aa90, v82
	ds_write_b16 v66, v71
	v_add_u32_e32 v66, 0x1aad0, v82
	ds_write_b16_d16_hi v66, v71
	v_add_u32_e32 v66, 0x1aea0, v82
	ds_write_b16 v66, v72
	v_add_u32_e32 v66, 0x1aee0, v82
	ds_write_b16_d16_hi v66, v72
	v_add_u32_e32 v66, 0x1b2b0, v82
	ds_write_b16 v66, v73
	v_add_u32_e32 v66, 0x1b2f0, v82
	ds_write_b16_d16_hi v66, v73
	v_add_u32_e32 v66, 0x1c700, v82
	ds_write_b16 v66, v74
	v_add_u32_e32 v66, 0x1c740, v82
	ds_write_b16_d16_hi v66, v74
	v_add_u32_e32 v66, 0x1cb10, v82
	ds_write_b16 v66, v75
	v_add_u32_e32 v66, 0x1cb50, v82
	ds_write_b16_d16_hi v66, v75
	v_add_u32_e32 v66, 0x1cf20, v82
	ds_write_b16 v66, v76
	v_add_u32_e32 v66, 0x1cf60, v82
	ds_write_b16_d16_hi v66, v76
	v_add_u32_e32 v66, 0x1d330, v82
	ds_write_b16 v66, v77
	v_add_u32_e32 v66, 0x1d370, v82
	ds_write_b16_d16_hi v66, v77
	v_add_u32_e32 v66, 0x1e780, v82
	ds_write_b16 v66, v78
	v_add_u32_e32 v66, 0x1e7c0, v82
	ds_write_b16_d16_hi v66, v78
	v_add_u32_e32 v66, 0x1eb90, v82
	ds_write_b16 v66, v79
	v_add_u32_e32 v66, 0x1ebd0, v82
	ds_write_b16_d16_hi v66, v79
	v_add_u32_e32 v66, 0x1efa0, v82
	v_add_u32_e32 v70, 0, v0
	v_xor_b32_e32 v0, 8, v234
	ds_write_b16 v66, v80
	v_add_u32_e32 v66, 0x1efe0, v82
	v_cmp_lt_i32_e32 vcc, v0, v104
	ds_write_b16_d16_hi v66, v80
	v_add_u32_e32 v66, 0x1f3b0, v82
	v_cndmask_b32_e32 v0, v234, v0, vcc
	s_mul_i32 s4, s12, 0x4100
	ds_write_b16 v66, v81
	v_add_u32_e32 v66, 0x1f3f0, v82
	v_lshlrev_b32_e32 v68, 2, v0
	v_xor_b32_e32 v0, 16, v234
	v_add_u32_e32 v69, s4, v70
	ds_write_b16_d16_hi v66, v81
	s_waitcnt lgkmcnt(0)
	s_barrier
	v_cmp_lt_i32_e32 vcc, v0, v104
	ds_read_b128 v[74:77], v69
	ds_read_b128 v[82:85], v69 offset:1040
	v_cndmask_b32_e32 v0, v234, v0, vcc
	v_lshlrev_b32_e32 v67, 2, v0
	v_xor_b32_e32 v0, 32, v234
	v_cmp_lt_i32_e32 vcc, v0, v104
	s_waitcnt vmcnt(15)
	v_lshlrev_b32_e32 v71, 16, v62
	v_and_b32_e32 v62, 0xffff0000, v62
	v_cndmask_b32_e32 v0, v234, v0, vcc
	v_lshlrev_b32_e32 v66, 2, v0
	s_waitcnt lgkmcnt(1)
	v_lshlrev_b32_e32 v0, 16, v74
	v_mul_f32_e32 v71, v71, v0
	v_and_b32_e32 v0, 0xffff0000, v74
	v_mul_f32_e32 v72, v62, v0
	v_lshlrev_b32_e32 v0, 16, v75
	v_lshlrev_b32_e32 v62, 16, v63
	v_mul_f32_e32 v73, v62, v0
	v_and_b32_e32 v0, 0xffff0000, v75
	v_and_b32_e32 v62, 0xffff0000, v63
	v_mul_f32_e32 v74, v62, v0
	v_lshlrev_b32_e32 v0, 16, v76
	v_lshlrev_b32_e32 v62, 16, v64
	v_mul_f32_e32 v62, v62, v0
	v_and_b32_e32 v0, 0xffff0000, v76
	v_and_b32_e32 v63, 0xffff0000, v64
	v_mul_f32_e32 v63, v63, v0
	v_lshlrev_b32_e32 v0, 16, v77
	v_lshlrev_b32_e32 v64, 16, v65
	v_mul_f32_e32 v64, v64, v0
	v_and_b32_e32 v0, 0xffff0000, v77
	v_and_b32_e32 v65, 0xffff0000, v65
	v_mul_f32_e32 v65, v65, v0
	s_waitcnt lgkmcnt(0)
	v_lshlrev_b32_e32 v0, 16, v82
	s_waitcnt vmcnt(14)
	v_lshlrev_b32_e32 v75, 16, v58
	v_mul_f32_e32 v79, v75, v0
	v_and_b32_e32 v0, 0xffff0000, v82
	v_and_b32_e32 v58, 0xffff0000, v58
	v_mul_f32_e32 v80, v58, v0
	v_lshlrev_b32_e32 v0, 16, v83
	v_lshlrev_b32_e32 v58, 16, v59
	v_mul_f32_e32 v81, v58, v0
	v_and_b32_e32 v0, 0xffff0000, v83
	v_and_b32_e32 v58, 0xffff0000, v59
	v_mul_f32_e32 v82, v58, v0
	v_lshlrev_b32_e32 v0, 16, v84
	v_lshlrev_b32_e32 v58, 16, v60
	v_mul_f32_e32 v75, v58, v0
	v_and_b32_e32 v0, 0xffff0000, v84
	v_and_b32_e32 v58, 0xffff0000, v60
	v_mul_f32_e32 v76, v58, v0
	v_lshlrev_b32_e32 v0, 16, v85
	v_lshlrev_b32_e32 v58, 16, v61
	v_mul_f32_e32 v77, v58, v0
	v_and_b32_e32 v0, 0xffff0000, v85
	ds_read_b128 v[84:87], v69 offset:2080
	ds_read_b128 v[90:93], v69 offset:3120
	v_and_b32_e32 v58, 0xffff0000, v61
	v_mul_f32_e32 v78, v58, v0
	s_waitcnt vmcnt(13)
	v_lshlrev_b32_e32 v58, 16, v54
	s_waitcnt lgkmcnt(1)
	v_lshlrev_b32_e32 v0, 16, v84
	v_mul_f32_e32 v58, v58, v0
	v_and_b32_e32 v0, 0xffff0000, v84
	v_and_b32_e32 v54, 0xffff0000, v54
	v_mul_f32_e32 v59, v54, v0
	v_lshlrev_b32_e32 v0, 16, v85
	v_lshlrev_b32_e32 v54, 16, v55
	v_mul_f32_e32 v60, v54, v0
	v_and_b32_e32 v0, 0xffff0000, v85
	v_and_b32_e32 v54, 0xffff0000, v55
	v_mul_f32_e32 v61, v54, v0
	v_lshlrev_b32_e32 v0, 16, v86
	v_lshlrev_b32_e32 v54, 16, v56
	v_mul_f32_e32 v54, v54, v0
	v_and_b32_e32 v0, 0xffff0000, v86
	v_and_b32_e32 v55, 0xffff0000, v56
	v_mul_f32_e32 v55, v55, v0
	v_lshlrev_b32_e32 v0, 16, v87
	v_lshlrev_b32_e32 v56, 16, v57
	v_mul_f32_e32 v56, v56, v0
	v_and_b32_e32 v0, 0xffff0000, v87
	v_and_b32_e32 v57, 0xffff0000, v57
	v_mul_f32_e32 v57, v57, v0
	s_waitcnt lgkmcnt(0)
	v_lshlrev_b32_e32 v0, 16, v90
	s_waitcnt vmcnt(12)
	v_lshlrev_b32_e32 v83, 16, v50
	v_mul_f32_e32 v87, v83, v0
	v_and_b32_e32 v0, 0xffff0000, v90
	v_and_b32_e32 v50, 0xffff0000, v50
	v_mul_f32_e32 v88, v50, v0
	v_lshlrev_b32_e32 v0, 16, v91
	v_lshlrev_b32_e32 v50, 16, v51
	v_mul_f32_e32 v89, v50, v0
	v_and_b32_e32 v0, 0xffff0000, v91
	v_and_b32_e32 v50, 0xffff0000, v51
	v_mul_f32_e32 v90, v50, v0
	v_lshlrev_b32_e32 v0, 16, v92
	v_lshlrev_b32_e32 v50, 16, v52
	v_mul_f32_e32 v83, v50, v0
	v_and_b32_e32 v0, 0xffff0000, v92
	v_and_b32_e32 v50, 0xffff0000, v52
	v_mul_f32_e32 v84, v50, v0
	v_lshlrev_b32_e32 v0, 16, v93
	v_lshlrev_b32_e32 v50, 16, v53
	v_mul_f32_e32 v85, v50, v0
	v_and_b32_e32 v0, 0xffff0000, v93
	ds_read_b128 v[92:95], v69 offset:4160
	ds_read_b128 v[104:107], v69 offset:5200
	v_and_b32_e32 v50, 0xffff0000, v53
	v_mul_f32_e32 v86, v50, v0
	s_waitcnt vmcnt(11)
	v_lshlrev_b32_e32 v50, 16, v46
	s_waitcnt lgkmcnt(1)
	v_lshlrev_b32_e32 v0, 16, v92
	v_mul_f32_e32 v50, v50, v0
	v_and_b32_e32 v0, 0xffff0000, v92
	v_and_b32_e32 v46, 0xffff0000, v46
	v_mul_f32_e32 v51, v46, v0
	v_lshlrev_b32_e32 v0, 16, v93
	v_lshlrev_b32_e32 v46, 16, v47
	v_mul_f32_e32 v52, v46, v0
	v_and_b32_e32 v0, 0xffff0000, v93
	v_and_b32_e32 v46, 0xffff0000, v47
	v_mul_f32_e32 v53, v46, v0
	v_lshlrev_b32_e32 v0, 16, v94
	v_lshlrev_b32_e32 v46, 16, v48
	v_mul_f32_e32 v46, v46, v0
	v_and_b32_e32 v0, 0xffff0000, v94
	v_and_b32_e32 v47, 0xffff0000, v48
	v_mul_f32_e32 v47, v47, v0
	v_lshlrev_b32_e32 v0, 16, v95
	v_lshlrev_b32_e32 v48, 16, v49
	v_mul_f32_e32 v48, v48, v0
	v_and_b32_e32 v0, 0xffff0000, v95
	v_and_b32_e32 v49, 0xffff0000, v49
	v_mul_f32_e32 v49, v49, v0
	s_waitcnt lgkmcnt(0)
	v_lshlrev_b32_e32 v0, 16, v104
	s_waitcnt vmcnt(10)
	v_lshlrev_b32_e32 v91, 16, v42
	v_mul_f32_e32 v95, v91, v0
	v_and_b32_e32 v0, 0xffff0000, v104
	v_and_b32_e32 v42, 0xffff0000, v42
	v_mul_f32_e32 v96, v42, v0
	v_lshlrev_b32_e32 v0, 16, v105
	v_lshlrev_b32_e32 v42, 16, v43
	v_mul_f32_e32 v97, v42, v0
	v_and_b32_e32 v0, 0xffff0000, v105
	v_and_b32_e32 v42, 0xffff0000, v43
	v_mul_f32_e32 v98, v42, v0
	v_lshlrev_b32_e32 v0, 16, v106
	v_lshlrev_b32_e32 v42, 16, v44
	v_mul_f32_e32 v91, v42, v0
	v_and_b32_e32 v0, 0xffff0000, v106
	v_and_b32_e32 v42, 0xffff0000, v44
	v_mul_f32_e32 v92, v42, v0
	v_lshlrev_b32_e32 v0, 16, v107
	v_lshlrev_b32_e32 v42, 16, v45
	v_mul_f32_e32 v93, v42, v0
	v_and_b32_e32 v0, 0xffff0000, v107
	ds_read_b128 v[104:107], v69 offset:6240
	ds_read_b128 v[108:111], v69 offset:7280
	v_and_b32_e32 v42, 0xffff0000, v45
	v_mul_f32_e32 v94, v42, v0
	s_waitcnt vmcnt(9)
	v_lshlrev_b32_e32 v42, 16, v38
	s_waitcnt lgkmcnt(1)
	v_lshlrev_b32_e32 v0, 16, v104
	v_mul_f32_e32 v42, v42, v0
	v_and_b32_e32 v0, 0xffff0000, v104
	v_and_b32_e32 v38, 0xffff0000, v38
	v_mul_f32_e32 v43, v38, v0
	v_lshlrev_b32_e32 v0, 16, v105
	v_lshlrev_b32_e32 v38, 16, v39
	v_mul_f32_e32 v44, v38, v0
	v_and_b32_e32 v0, 0xffff0000, v105
	v_and_b32_e32 v38, 0xffff0000, v39
	v_mul_f32_e32 v45, v38, v0
	v_lshlrev_b32_e32 v0, 16, v106
	v_lshlrev_b32_e32 v38, 16, v40
	v_mul_f32_e32 v38, v38, v0
	v_and_b32_e32 v0, 0xffff0000, v106
	v_and_b32_e32 v39, 0xffff0000, v40
	v_mul_f32_e32 v39, v39, v0
	v_lshlrev_b32_e32 v0, 16, v107
	v_lshlrev_b32_e32 v40, 16, v41
	v_mul_f32_e32 v40, v40, v0
	v_and_b32_e32 v0, 0xffff0000, v107
	v_and_b32_e32 v41, 0xffff0000, v41
	v_mul_f32_e32 v41, v41, v0
	s_waitcnt lgkmcnt(0)
	v_lshlrev_b32_e32 v0, 16, v108
	s_waitcnt vmcnt(8)
	v_lshlrev_b32_e32 v99, 16, v34
	v_mul_f32_e32 v105, v99, v0
	v_and_b32_e32 v0, 0xffff0000, v108
	v_and_b32_e32 v34, 0xffff0000, v34
	v_mul_f32_e32 v106, v34, v0
	v_lshlrev_b32_e32 v0, 16, v109
	v_lshlrev_b32_e32 v34, 16, v35
	v_mul_f32_e32 v107, v34, v0
	v_and_b32_e32 v0, 0xffff0000, v109
	v_and_b32_e32 v34, 0xffff0000, v35
	v_mul_f32_e32 v108, v34, v0
	v_lshlrev_b32_e32 v0, 16, v110
	v_lshlrev_b32_e32 v34, 16, v36
	v_mul_f32_e32 v99, v34, v0
	v_and_b32_e32 v0, 0xffff0000, v110
	v_and_b32_e32 v34, 0xffff0000, v36
	v_mul_f32_e32 v36, v34, v0
	v_lshlrev_b32_e32 v0, 16, v111
	v_lshlrev_b32_e32 v34, 16, v37
	v_mul_f32_e32 v104, v34, v0
	v_and_b32_e32 v0, 0xffff0000, v111
	v_and_b32_e32 v34, 0xffff0000, v37
	v_mul_f32_e32 v37, v34, v0
	v_max3_f32 v0, |v71|, 0, |v72|
	v_max3_f32 v0, v0, |v73|, |v74|
	v_max3_f32 v0, v0, |v62|, |v63|
	v_max3_f32 v0, v0, |v64|, |v65|
	s_nop 1
	v_max_f32_dpp v0, v0, v0 quad_perm:[1,0,3,2] row_mask:0xf bank_mask:0xf
	s_nop 1
	v_max_f32_dpp v0, v0, v0 quad_perm:[2,3,0,1] row_mask:0xf bank_mask:0xf
	s_nop 1
	v_max_f32_dpp v0, v0, v0 row_half_mirror row_mask:0xf bank_mask:0xf
	s_nop 1
	v_max_f32_dpp v0, v0, v0 row_ror:8 row_mask:0xf bank_mask:0xf
	v_mov_b32_e32 v114, v0
	s_nop 1
	v_permlane16_swap_b32_e32 v0, v114
	s_nop 0
	v_max_f32_e32 v0, v0, v114
	v_mov_b32_e32 v114, v0
	s_nop 1
	v_permlane32_swap_b32_e32 v0, v114
	s_nop 0
	v_max_f32_e32 v0, v0, v114
	v_mov_b32_e32 v114, v0
	v_max3_f32 v34, |v79|, 0, |v80|
	v_max3_f32 v34, v34, |v81|, |v82|
	v_max3_f32 v34, v34, |v75|, |v76|
	v_max3_f32 v34, v34, |v77|, |v78|
	s_waitcnt lgkmcnt(0)
	v_max_f32_e32 v114, v114, v114
	v_max_f32_e32 v0, v0, v114
	s_nop 1
	v_max_f32_dpp v34, v34, v34 quad_perm:[1,0,3,2] row_mask:0xf bank_mask:0xf
	s_nop 1
	v_max_f32_dpp v34, v34, v34 quad_perm:[2,3,0,1] row_mask:0xf bank_mask:0xf
	s_nop 1
	v_max_f32_dpp v34, v34, v34 row_half_mirror row_mask:0xf bank_mask:0xf
	s_nop 1
	v_max_f32_dpp v34, v34, v34 row_ror:8 row_mask:0xf bank_mask:0xf
	v_mov_b32_e32 v114, v34
	s_nop 1
	v_permlane16_swap_b32_e32 v34, v114
	s_nop 0
	v_max_f32_e32 v34, v34, v114
	v_mov_b32_e32 v114, v34
	s_nop 1
	v_permlane32_swap_b32_e32 v34, v114
	s_nop 0
	v_max_f32_e32 v34, v34, v114
	v_mov_b32_e32 v114, v34
	v_max3_f32 v35, |v58|, 0, |v59|
	v_max3_f32 v35, v35, |v60|, |v61|
	v_max3_f32 v35, v35, |v54|, |v55|
	v_max3_f32 v35, v35, |v56|, |v57|
	s_waitcnt lgkmcnt(0)
	v_max_f32_e32 v114, v114, v114
	v_max_f32_e32 v34, v34, v114
	s_nop 1
	v_max_f32_dpp v35, v35, v35 quad_perm:[1,0,3,2] row_mask:0xf bank_mask:0xf
	s_nop 1
	v_max_f32_dpp v35, v35, v35 quad_perm:[2,3,0,1] row_mask:0xf bank_mask:0xf
	s_nop 1
	v_max_f32_dpp v35, v35, v35 row_half_mirror row_mask:0xf bank_mask:0xf
	s_nop 1
	v_max_f32_dpp v35, v35, v35 row_ror:8 row_mask:0xf bank_mask:0xf
	v_mov_b32_e32 v114, v35
	s_nop 1
	v_permlane16_swap_b32_e32 v35, v114
	s_nop 0
	v_max_f32_e32 v35, v35, v114
	v_mov_b32_e32 v114, v35
	s_nop 1
	v_permlane32_swap_b32_e32 v35, v114
	s_nop 0
	v_max_f32_e32 v35, v35, v114
	v_mov_b32_e32 v114, v35
	v_max3_f32 v109, |v87|, 0, |v88|
	v_max3_f32 v109, v109, |v89|, |v90|
	v_max3_f32 v109, v109, |v83|, |v84|
	v_max3_f32 v109, v109, |v85|, |v86|
	s_waitcnt lgkmcnt(0)
	v_max_f32_e32 v114, v114, v114
	v_max_f32_e32 v35, v35, v114
	s_nop 1
	v_max_f32_dpp v109, v109, v109 quad_perm:[1,0,3,2] row_mask:0xf bank_mask:0xf
	s_nop 1
	v_max_f32_dpp v109, v109, v109 quad_perm:[2,3,0,1] row_mask:0xf bank_mask:0xf
	s_nop 1
	v_max_f32_dpp v109, v109, v109 row_half_mirror row_mask:0xf bank_mask:0xf
	s_nop 1
	v_max_f32_dpp v109, v109, v109 row_ror:8 row_mask:0xf bank_mask:0xf
	v_mov_b32_e32 v114, v109
	s_nop 1
	v_permlane16_swap_b32_e32 v109, v114
	s_nop 0
	v_max_f32_e32 v109, v109, v114
	v_mov_b32_e32 v114, v109
	s_nop 1
	v_permlane32_swap_b32_e32 v109, v114
	s_nop 0
	v_max_f32_e32 v109, v109, v114
	v_mov_b32_e32 v114, v109
	v_max3_f32 v110, |v50|, 0, |v51|
	v_max3_f32 v110, v110, |v52|, |v53|
	v_max3_f32 v110, v110, |v46|, |v47|
	v_max3_f32 v110, v110, |v48|, |v49|
	s_waitcnt lgkmcnt(0)
	v_max_f32_e32 v114, v114, v114
	v_max_f32_e32 v109, v109, v114
	s_nop 1
	v_max_f32_dpp v110, v110, v110 quad_perm:[1,0,3,2] row_mask:0xf bank_mask:0xf
	s_nop 1
	v_max_f32_dpp v110, v110, v110 quad_perm:[2,3,0,1] row_mask:0xf bank_mask:0xf
	s_nop 1
	v_max_f32_dpp v110, v110, v110 row_half_mirror row_mask:0xf bank_mask:0xf
	s_nop 1
	v_max_f32_dpp v110, v110, v110 row_ror:8 row_mask:0xf bank_mask:0xf
	v_mov_b32_e32 v114, v110
	s_nop 1
	v_permlane16_swap_b32_e32 v110, v114
	s_nop 0
	v_max_f32_e32 v110, v110, v114
	v_mov_b32_e32 v114, v110
	s_nop 1
	v_permlane32_swap_b32_e32 v110, v114
	s_nop 0
	v_max_f32_e32 v110, v110, v114
	v_mov_b32_e32 v114, v110
	v_max3_f32 v111, |v95|, 0, |v96|
	v_max3_f32 v111, v111, |v97|, |v98|
	v_max3_f32 v111, v111, |v91|, |v92|
	v_max3_f32 v111, v111, |v93|, |v94|
	s_waitcnt lgkmcnt(0)
	v_max_f32_e32 v114, v114, v114
	v_max_f32_e32 v110, v110, v114
	s_nop 1
	v_max_f32_dpp v111, v111, v111 quad_perm:[1,0,3,2] row_mask:0xf bank_mask:0xf
	s_nop 1
	v_max_f32_dpp v111, v111, v111 quad_perm:[2,3,0,1] row_mask:0xf bank_mask:0xf
	s_nop 1
	v_max_f32_dpp v111, v111, v111 row_half_mirror row_mask:0xf bank_mask:0xf
	s_nop 1
	v_max_f32_dpp v111, v111, v111 row_ror:8 row_mask:0xf bank_mask:0xf
	v_mov_b32_e32 v114, v111
	s_nop 1
	v_permlane16_swap_b32_e32 v111, v114
	s_nop 0
	v_max_f32_e32 v111, v111, v114
	v_mov_b32_e32 v114, v111
	s_nop 1
	v_permlane32_swap_b32_e32 v111, v114
	s_nop 0
	v_max_f32_e32 v111, v111, v114
	v_mov_b32_e32 v114, v111
	v_max3_f32 v112, |v42|, 0, |v43|
	v_max3_f32 v112, v112, |v44|, |v45|
	v_max3_f32 v112, v112, |v38|, |v39|
	v_max3_f32 v112, v112, |v40|, |v41|
	s_waitcnt lgkmcnt(0)
	v_max_f32_e32 v114, v114, v114
	v_max_f32_e32 v111, v111, v114
	s_nop 1
	v_max_f32_dpp v112, v112, v112 quad_perm:[1,0,3,2] row_mask:0xf bank_mask:0xf
	s_nop 1
	v_max_f32_dpp v112, v112, v112 quad_perm:[2,3,0,1] row_mask:0xf bank_mask:0xf
	s_nop 1
	v_max_f32_dpp v112, v112, v112 row_half_mirror row_mask:0xf bank_mask:0xf
	s_nop 1
	v_max_f32_dpp v112, v112, v112 row_ror:8 row_mask:0xf bank_mask:0xf
	v_mov_b32_e32 v114, v112
	s_nop 1
	v_permlane16_swap_b32_e32 v112, v114
	s_nop 0
	v_max_f32_e32 v112, v112, v114
	v_mov_b32_e32 v114, v112
	s_nop 1
	v_permlane32_swap_b32_e32 v112, v114
	s_nop 0
	v_max_f32_e32 v112, v112, v114
	v_mov_b32_e32 v114, v112
	v_max3_f32 v113, |v105|, 0, |v106|
	v_max3_f32 v113, v113, |v107|, |v108|
	v_max3_f32 v113, v113, |v99|, |v36|
	v_max3_f32 v113, v113, |v104|, |v37|
	s_waitcnt lgkmcnt(0)
	v_max_f32_e32 v114, v114, v114
	v_max_f32_e32 v112, v112, v114
	s_nop 1
	v_max_f32_dpp v113, v113, v113 quad_perm:[1,0,3,2] row_mask:0xf bank_mask:0xf
	s_nop 1
	v_max_f32_dpp v113, v113, v113 quad_perm:[2,3,0,1] row_mask:0xf bank_mask:0xf
	s_nop 1
	v_max_f32_dpp v113, v113, v113 row_half_mirror row_mask:0xf bank_mask:0xf
	s_nop 1
	v_max_f32_dpp v113, v113, v113 row_ror:8 row_mask:0xf bank_mask:0xf
	v_mov_b32_e32 v114, v113
	s_nop 1
	v_permlane16_swap_b32_e32 v113, v114
	s_nop 0
	v_max_f32_e32 v113, v113, v114
	v_mov_b32_e32 v114, v113
	s_nop 1
	v_permlane32_swap_b32_e32 v113, v114
	s_nop 0
	v_max_f32_e32 v113, v113, v114
	v_mov_b32_e32 v114, v113
	s_waitcnt lgkmcnt(0)
	v_max_f32_e32 v114, v114, v114
	v_max_f32_e32 v113, v113, v114
	v_mov_b32_e32 v114, v0
	s_waitcnt lgkmcnt(0)
	v_max_f32_e32 v114, v114, v114
	v_max_f32_e32 v0, v0, v114
	v_mov_b32_e32 v114, v34
	s_waitcnt lgkmcnt(0)
	v_max_f32_e32 v114, v114, v114
	v_max_f32_e32 v34, v34, v114
	v_mov_b32_e32 v114, v35
	s_waitcnt lgkmcnt(0)
	v_max_f32_e32 v114, v114, v114
	v_max_f32_e32 v35, v35, v114
	v_mov_b32_e32 v114, v109
	s_waitcnt lgkmcnt(0)
	v_max_f32_e32 v114, v114, v114
	v_max_f32_e32 v109, v109, v114
	v_mov_b32_e32 v114, v110
	s_waitcnt lgkmcnt(0)
	v_max_f32_e32 v114, v114, v114
	v_max_f32_e32 v110, v110, v114
	v_mov_b32_e32 v114, v111
	s_waitcnt lgkmcnt(0)
	v_max_f32_e32 v114, v114, v114
	v_max_f32_e32 v111, v111, v114
	v_mov_b32_e32 v114, v112
	s_waitcnt lgkmcnt(0)
	v_max_f32_e32 v114, v114, v114
	v_max_f32_e32 v112, v112, v114
	v_mov_b32_e32 v114, v113
	s_waitcnt lgkmcnt(0)
	v_max_f32_e32 v114, v114, v114
	v_max_f32_e32 v113, v113, v114
	v_mov_b32_e32 v114, v0
	s_waitcnt lgkmcnt(0)
	v_max_f32_e32 v114, v114, v114
	v_max_f32_e32 v0, v0, v114
	v_mov_b32_e32 v114, v34
	s_waitcnt lgkmcnt(0)
	v_max_f32_e32 v114, v114, v114
	v_max_f32_e32 v34, v34, v114
	v_mov_b32_e32 v114, v35
	s_waitcnt lgkmcnt(0)
	v_max_f32_e32 v114, v114, v114
	v_max_f32_e32 v35, v35, v114
	v_mov_b32_e32 v114, v109
	s_waitcnt lgkmcnt(0)
	v_max_f32_e32 v114, v114, v114
	v_max_f32_e32 v109, v109, v114
	v_mov_b32_e32 v114, v110
	s_waitcnt lgkmcnt(0)
	v_max_f32_e32 v114, v114, v114
	v_max_f32_e32 v110, v110, v114
	v_mov_b32_e32 v114, v111
	s_waitcnt lgkmcnt(0)
	v_max_f32_e32 v114, v114, v114
	v_max_f32_e32 v111, v111, v114
	v_mov_b32_e32 v114, v112
	s_waitcnt lgkmcnt(0)
	v_max_f32_e32 v114, v114, v114
	v_max_f32_e32 v112, v112, v114
	v_mov_b32_e32 v114, v113
	s_waitcnt lgkmcnt(0)
	v_max_f32_e32 v114, v114, v114
	v_max_f32_e32 v113, v113, v114
	v_mov_b32_e32 v114, v0
	s_waitcnt lgkmcnt(0)
	v_max_f32_e32 v114, v114, v114
	v_max_f32_e32 v0, v0, v114
	v_mov_b32_e32 v114, v34
	s_waitcnt lgkmcnt(0)
	v_max_f32_e32 v114, v114, v114
	v_max_f32_e32 v34, v34, v114
	v_mov_b32_e32 v114, v35
	s_waitcnt lgkmcnt(0)
	v_max_f32_e32 v114, v114, v114
	v_max_f32_e32 v35, v35, v114
	v_mov_b32_e32 v114, v109
	s_waitcnt lgkmcnt(0)
	v_max_f32_e32 v114, v114, v114
	v_max_f32_e32 v109, v109, v114
	v_mov_b32_e32 v114, v110
	s_waitcnt lgkmcnt(0)
	v_max_f32_e32 v114, v114, v114
	v_max_f32_e32 v110, v110, v114
	v_mov_b32_e32 v114, v111
	s_waitcnt lgkmcnt(0)
	v_max_f32_e32 v114, v114, v114
	v_max_f32_e32 v111, v111, v114
	v_mov_b32_e32 v114, v112
	s_waitcnt lgkmcnt(0)
	v_max_f32_e32 v114, v114, v114
	v_max_f32_e32 v112, v112, v114
	v_mov_b32_e32 v114, v113
	s_waitcnt lgkmcnt(0)
	v_max_f32_e32 v114, v114, v114
	v_max_f32_e32 v114, v113, v114
	v_mov_b32_e32 v113, v0
	s_waitcnt lgkmcnt(0)
	v_max_f32_e32 v113, v113, v113
	v_max_f32_e32 v0, v0, v113
	v_mov_b32_e32 v113, v34
	s_waitcnt lgkmcnt(0)
	v_max_f32_e32 v113, v113, v113
	v_max_f32_e32 v120, v34, v113
	v_mov_b32_e32 v34, v35
	v_mov_b32_e32 v122, v120
	s_waitcnt lgkmcnt(0)
	v_max_f32_e32 v34, v34, v34
	v_max_f32_e32 v118, v35, v34
	v_mov_b32_e32 v34, v109
	v_mov_b32_e32 v121, v118
	s_waitcnt lgkmcnt(0)
	v_max_f32_e32 v34, v34, v34
	v_max_f32_e32 v116, v109, v34
	v_mov_b32_e32 v34, v110
	v_mov_b32_e32 v119, v116
	s_waitcnt lgkmcnt(0)
	v_max_f32_e32 v34, v34, v34
	v_max_f32_e32 v115, v110, v34
	v_mov_b32_e32 v34, v111
	v_mov_b32_e32 v117, v115
	s_waitcnt lgkmcnt(0)
	v_max_f32_e32 v34, v34, v34
	v_max_f32_e32 v113, v111, v34
	v_mov_b32_e32 v34, v112
	s_waitcnt lgkmcnt(0)
	v_max_f32_e32 v34, v34, v34
	v_max_f32_e32 v111, v112, v34
	v_mov_b32_e32 v34, v114
	v_mov_b32_e32 v112, v111
	s_waitcnt lgkmcnt(0)
	v_max_f32_e32 v34, v34, v34
	v_max_f32_e32 v109, v114, v34
	v_mov_b32_e32 v34, v0
	v_mov_b32_e32 v114, v113
	v_mov_b32_e32 v110, v109
	s_waitcnt lgkmcnt(0)
	v_max3_f32 v123, v0, v34, s72
	s_and_saveexec_b64 s[12:13], s[6:7]
	s_cbranch_execz .LBB0_490
	s_lshl_b64 s[4:5], s[16:17], 2
	s_add_u32 s4, s18, s4
	s_addc_u32 s5, s19, s5
	v_mul_f32_e32 v0, 0x3c010204, v123
	global_store_dword v1, v0, s[4:5]
